# v79 + 1/sqrt in the rms-norm rows as v_rsq_f32 + one Newton step (f32) instead of hipcc's IEEE sqrt+div expansion
# speedup vs baseline: 1.0085x; 1.0036x over previous
; __device__ __forceinline__ unsigned pk2(float lo, float hi) { const pk_f2 v = {lo, hi}; return __builtin_bit_cast(unsigned, __builtin_convertvector(v, pk_b2)); }
; template <class AP> __device__ __forceinline__ void phase_prologue(const AP a, LAS unsigned char* lds, int tid, int lane, int wave, int vcu, int G) {
;     ...
;       for (int rp = rpa; rp < M / 2; rp += rps) {
;           const int row = 2 * rp + h5; const unsigned vo = (unsigned)row * (DM * 4) + (unsigned)l31 * 32u, vob = (unsigned)row * (DM * 2) + (unsigned)l31 * 16u;
;           v4u q0[8], q1[8];
; #pragma unroll
;           for (int j = 0; j < 8; ++j) { q0[j] = __builtin_amdgcn_raw_buffer_load_b128(rsX, vo, (unsigned)j * 1024u, 0); q1[j] = __builtin_amdgcn_raw_buffer_load_b128(rsX, vo, (unsigned)j * 1024u + 16u, 0); }
;           float ss = 0.f;
; #pragma unroll
;           for (int j = 0; j < 8; ++j) { const f32x4 p = __builtin_bit_cast(f32x4, q0[j]), c = __builtin_bit_cast(f32x4, q1[j]);
;               ss += ((p.x * p.x + p.y * p.y) + (p.z * p.z + p.w * p.w)) + ((c.x * c.x + c.y * c.y) + (c.z * c.z + c.w * c.w));
;               v4u o; o.x = pk2(p.x, p.y); o.y = pk2(p.z, p.w); o.z = pk2(c.x, c.y); o.w = pk2(c.z, c.w);
;               __builtin_amdgcn_raw_buffer_store_b128(o, rsC, vob, (unsigned)j * 512u, 0); }
;           ss = half_sum(ss);
;           if (l31 == 0) ((float*)(ws + WS_XRS))[row] = 1.0f / sqrtf(ss * (1.0f / DM) + EPS);
;       }
.LBB0_168:
	buffer_load_dwordx4 v[6:9], v3, s[12:15], 0 offen
	buffer_load_dwordx4 v[10:13], v3, s[12:15], 16 offen
	buffer_load_dwordx4 v[14:17], v3, s[12:15], s25 offen
	buffer_load_dwordx4 v[18:21], v3, s[12:15], s26 offen
	buffer_load_dwordx4 v[22:25], v3, s[12:15], s27 offen
	buffer_load_dwordx4 v[26:29], v3, s[12:15], s28 offen
	buffer_load_dwordx4 v[30:33], v3, s[12:15], s29 offen
	buffer_load_dwordx4 v[34:37], v3, s[12:15], s30 offen
	buffer_load_dwordx4 v[38:41], v3, s[12:15], s31 offen
	buffer_load_dwordx4 v[42:45], v3, s[12:15], s34 offen
	buffer_load_dwordx4 v[46:49], v3, s[12:15], s35 offen
	buffer_load_dwordx4 v[50:53], v3, s[12:15], s36 offen
	buffer_load_dwordx4 v[54:57], v3, s[12:15], s37 offen
	buffer_load_dwordx4 v[58:61], v3, s[12:15], s38 offen
	buffer_load_dwordx4 v[62:65], v3, s[12:15], s39 offen
	buffer_load_dwordx4 v[66:69], v3, s[12:15], s40 offen
	s_waitcnt vmcnt(15)
	v_mul_f32_e32 v1, v7, v7
	v_mul_f32_e32 v86, v9, v9
	s_waitcnt vmcnt(14)
	v_mul_f32_e32 v87, v11, v11
	v_mul_f32_e32 v88, v13, v13
	v_cvt_pk_bf16_f32 v70, v6, v7
	v_cvt_pk_bf16_f32 v71, v8, v9
	v_cvt_pk_bf16_f32 v72, v10, v11
	v_cvt_pk_bf16_f32 v73, v12, v13
	s_waitcnt vmcnt(13)
	v_mul_f32_e32 v7, v15, v15
	v_mul_f32_e32 v9, v17, v17
	s_waitcnt vmcnt(12)
	v_mul_f32_e32 v11, v19, v19
	v_mul_f32_e32 v13, v21, v21
	v_cvt_pk_bf16_f32 v74, v14, v15
	v_cvt_pk_bf16_f32 v75, v16, v17
	v_cvt_pk_bf16_f32 v76, v18, v19
	v_cvt_pk_bf16_f32 v77, v20, v21
	s_waitcnt vmcnt(11)
	v_mul_f32_e32 v15, v23, v23
	v_mul_f32_e32 v17, v25, v25
	s_waitcnt vmcnt(10)
	v_mul_f32_e32 v19, v27, v27
	v_mul_f32_e32 v21, v29, v29
	v_fmac_f32_e32 v1, v6, v6
	v_fmac_f32_e32 v86, v8, v8
	v_fmac_f32_e32 v87, v10, v10
	v_fmac_f32_e32 v88, v12, v12
	v_fmac_f32_e32 v7, v14, v14
	v_fmac_f32_e32 v9, v16, v16
	v_fmac_f32_e32 v11, v18, v18
	v_fmac_f32_e32 v13, v20, v20
	v_cvt_pk_bf16_f32 v78, v22, v23
	v_cvt_pk_bf16_f32 v79, v24, v25
	v_cvt_pk_bf16_f32 v80, v26, v27
	v_cvt_pk_bf16_f32 v81, v28, v29
	s_waitcnt vmcnt(9)
	v_mul_f32_e32 v23, v31, v31
	v_mul_f32_e32 v25, v33, v33
	s_waitcnt vmcnt(8)
	v_mul_f32_e32 v27, v35, v35
	v_mul_f32_e32 v29, v37, v37
	v_fmac_f32_e32 v15, v22, v22
	v_fmac_f32_e32 v17, v24, v24
	v_fmac_f32_e32 v19, v26, v26
	v_fmac_f32_e32 v21, v28, v28
	v_add_f32_e32 v1, v1, v86
	v_add_f32_e32 v6, v87, v88
	v_add_f32_e32 v7, v7, v9
	v_add_f32_e32 v8, v11, v13
	v_fmac_f32_e32 v23, v30, v30
	v_fmac_f32_e32 v25, v32, v32
	v_fmac_f32_e32 v27, v34, v34
	v_fmac_f32_e32 v29, v36, v36
	v_add_f32_e32 v9, v15, v17
	v_add_f32_e32 v10, v19, v21
	v_add_f32_e32 v1, v1, v6
	v_add_f32_e32 v6, v7, v8
	v_add_f32_e32 v11, v23, v25
	v_add_f32_e32 v12, v27, v29
	v_add_f32_e32 v7, v9, v10
	v_add_f32_e32 v1, v1, v6
	v_add_f32_e32 v8, v11, v12
	v_add_f32_e32 v1, v1, v7
	v_cvt_pk_bf16_f32 v82, v30, v31
	v_cvt_pk_bf16_f32 v83, v32, v33
	s_waitcnt vmcnt(7)
	v_mul_f32_e32 v31, v39, v39
	v_mul_f32_e32 v33, v41, v41
	v_add_f32_e32 v1, v1, v8
	s_waitcnt vmcnt(6)
	v_mul_f32_e32 v7, v43, v43
	v_mul_f32_e32 v8, v45, v45
	v_fmac_f32_e32 v31, v38, v38
	v_fmac_f32_e32 v33, v40, v40
	v_fmac_f32_e32 v7, v42, v42
	v_fmac_f32_e32 v8, v44, v44
	v_add_f32_e32 v6, v31, v33
	v_add_f32_e32 v7, v7, v8
	v_add_f32_e32 v6, v6, v7
	v_cvt_pk_bf16_f32 v84, v34, v35
	v_cvt_pk_bf16_f32 v85, v36, v37
	v_add_f32_e32 v1, v1, v6
	v_cvt_pk_bf16_f32 v6, v38, v39
	v_cvt_pk_bf16_f32 v7, v40, v41
	v_cvt_pk_bf16_f32 v8, v42, v43
	v_cvt_pk_bf16_f32 v9, v44, v45
	buffer_store_dwordx4 v[70:73], v2, s[16:19], 0 offen
	buffer_store_dwordx4 v[74:77], v2, s[16:19], s20 offen
	buffer_store_dwordx4 v[78:81], v2, s[16:19], s25 offen
	buffer_store_dwordx4 v[82:85], v2, s[16:19], s41 offen
	buffer_store_dwordx4 v[6:9], v2, s[16:19], s27 offen
	s_waitcnt vmcnt(10)
	v_mul_f32_e32 v6, v47, v47
	v_mul_f32_e32 v7, v49, v49
	v_fmac_f32_e32 v6, v46, v46
	v_fmac_f32_e32 v7, v48, v48
	v_add_f32_e32 v6, v6, v7
	s_waitcnt vmcnt(9)
	v_mul_f32_e32 v7, v51, v51
	v_mul_f32_e32 v8, v53, v53
	v_fmac_f32_e32 v7, v50, v50
	v_fmac_f32_e32 v8, v52, v52
	v_add_f32_e32 v7, v7, v8
	v_add_f32_e32 v6, v6, v7
	v_add_f32_e32 v1, v1, v6
	v_cvt_pk_bf16_f32 v6, v46, v47
	v_cvt_pk_bf16_f32 v7, v48, v49
	v_cvt_pk_bf16_f32 v8, v50, v51
	v_cvt_pk_bf16_f32 v9, v52, v53
	buffer_store_dwordx4 v[6:9], v2, s[16:19], s42 offen
	s_waitcnt vmcnt(9)
	v_mul_f32_e32 v6, v55, v55
	v_mul_f32_e32 v7, v57, v57
	v_fmac_f32_e32 v6, v54, v54
	v_fmac_f32_e32 v7, v56, v56
	v_add_f32_e32 v6, v6, v7
	s_waitcnt vmcnt(8)
	v_mul_f32_e32 v7, v59, v59
	v_mul_f32_e32 v8, v61, v61
	v_fmac_f32_e32 v7, v58, v58
	v_fmac_f32_e32 v8, v60, v60
	v_add_f32_e32 v7, v7, v8
	v_add_f32_e32 v6, v6, v7
	v_add_f32_e32 v1, v1, v6
	v_cvt_pk_bf16_f32 v6, v54, v55
	v_cvt_pk_bf16_f32 v7, v56, v57
	v_cvt_pk_bf16_f32 v8, v58, v59
	v_cvt_pk_bf16_f32 v9, v60, v61
	buffer_store_dwordx4 v[6:9], v2, s[16:19], s29 offen
	s_waitcnt vmcnt(8)
	v_mul_f32_e32 v6, v63, v63
	v_mul_f32_e32 v7, v65, v65
	v_fmac_f32_e32 v6, v62, v62
	v_fmac_f32_e32 v7, v64, v64
	v_add_f32_e32 v6, v6, v7
	s_waitcnt vmcnt(7)
	v_mul_f32_e32 v7, v67, v67
	v_mul_f32_e32 v8, v69, v69
	v_fmac_f32_e32 v7, v66, v66
	v_fmac_f32_e32 v8, v68, v68
	v_add_f32_e32 v7, v7, v8
	v_add_f32_e32 v6, v6, v7
	v_add_f32_e32 v1, v1, v6
	v_cvt_pk_bf16_f32 v6, v62, v63
	v_cvt_pk_bf16_f32 v7, v64, v65
	v_add_f32_dpp v1, v1, v1 quad_perm:[1,0,3,2] row_mask:0xf bank_mask:0xf bound_ctrl:1
	v_cvt_pk_bf16_f32 v8, v66, v67
	v_cvt_pk_bf16_f32 v9, v68, v69
	v_add_f32_dpp v1, v1, v1 quad_perm:[2,3,0,1] row_mask:0xf bank_mask:0xf bound_ctrl:1
	buffer_store_dwordx4 v[6:9], v2, s[16:19], s43 offen
	s_nop 0
	v_add_f32_dpp v1, v1, v1 row_half_mirror row_mask:0xf bank_mask:0xf bound_ctrl:1
	s_nop 1
	v_add_f32_dpp v1, v1, v1 row_mirror row_mask:0xf bank_mask:0xf bound_ctrl:1
	s_nop 0
	v_readlane_b32 s8, v1, 0
	v_readlane_b32 s46, v1, 16
	v_readlane_b32 s9, v1, 32
	v_readlane_b32 s47, v1, 48
	s_and_saveexec_b64 s[2:3], s[6:7]
	s_cbranch_execz .LBB0_167
	v_mov_b32_e32 v1, s46
	v_mov_b32_e32 v6, s47
	v_add_f32_e32 v1, s8, v1
	v_add_f32_e32 v6, s9, v6
	v_cndmask_b32_e64 v1, v6, v1, s[4:5]
	v_fmamk_f32 v1, v1, 0x3a000000, v4
	v_mul_f32_e32 v6, 0x4f800000, v1
	v_rsq_f32_e32 v6, v1
	s_nop 0
	v_mul_f32_e32 v7, v1, v6
	v_fma_f32 v7, -v7, v6, 1.0
	v_mul_f32_e32 v9, 0.5, v6
	v_fma_f32 v8, v9, v7, v6
	v_ashrrev_i32_e32 v1, 31, v0
	v_lshl_add_u64 v[6:7], v[0:1], 2, s[0:1]
	global_store_dword v[6:7], v8, off
	s_branch .LBB0_167

; #define GAS __attribute__((address_space(1)))
; __device__ __forceinline__ void phase_normmod_bf(const bf16* hin, const float* g, const float* shift, const float* scale  , bf16* U, int gw, int NGW, int lane) {
;     ...
;         for (int rr = 0; rr < 8; ++rr) {
;             const GAS v4u* xr = (const GAS v4u*)(hin + (size_t)(r0 + rr) * DM) + lane;
;             f32x4 v[8]; float ss = 0.f;
; #pragma unroll
;             for (int j = 0; j < 4; ++j) { const v4u q = xr[64 * j]; v[2 * j] = (f32x4){bflo(q.x), bfhi(q.x), bflo(q.y), bfhi(q.y)}; v[2 * j + 1] = (f32x4){bflo(q.z), bfhi(q.z), bflo(q.w), bfhi(q.w)}; }
; #pragma unroll
;             for (int j = 0; j < 8; ++j) ss += (v[j].x * v[j].x + v[j].y * v[j].y) + (v[j].z * v[j].z + v[j].w * v[j].w);
.LBB0_232:
	s_nop 0
	v_lshl_add_u64 v[88:89], v[46:47], 0, s[8:9]
	global_load_dwordx4 v[114:117], v[88:89], off
	global_load_dwordx4 v[118:121], v[88:89], off offset:1024
	global_load_dwordx4 v[106:109], v[88:89], off offset:2048
	global_load_dwordx4 v[122:125], v[88:89], off offset:3072
	s_waitcnt vmcnt(3)
	v_and_b32_e32 v113, 0xffff0000, v117
	s_waitcnt vmcnt(2)
	v_lshlrev_b32_e32 v98, 16, v120
	v_and_b32_e32 v99, 0xffff0000, v120
	s_waitcnt vmcnt(1)
	v_lshlrev_b32_e32 v94, 16, v106
	v_and_b32_e32 v120, 0xffff0000, v106
	v_lshlrev_b32_e32 v96, 16, v107
	v_and_b32_e32 v97, 0xffff0000, v107
	v_and_b32_e32 v107, 0xffff0000, v116
	v_and_b32_e32 v106, 0xffff0000, v114
	v_and_b32_e32 v112, 0xffff0000, v115
	v_lshlrev_b32_e32 v103, 16, v116
	v_lshlrev_b32_e32 v102, 16, v114
	v_lshlrev_b32_e32 v111, 16, v117
	v_lshlrev_b32_e32 v110, 16, v115
	v_pk_mul_f32 v[100:101], v[106:107], v[106:107]
	v_pk_mul_f32 v[104:105], v[112:113], v[112:113]
	v_pk_fma_f32 v[100:101], v[102:103], v[102:103], v[100:101]
	v_pk_fma_f32 v[104:105], v[110:111], v[110:111], v[104:105]
	s_waitcnt vmcnt(0)
; #define GAS __attribute__((address_space(1)))
; __device__ __forceinline__ unsigned pk2(float lo, float hi) { const pk_f2 v = {lo, hi}; return __builtin_bit_cast(unsigned, __builtin_convertvector(v, pk_b2)); }
; __device__ __forceinline__ float wave_sum(float v) { v = row16_sum(v); return (WS_RL(v, 0) + WS_RL(v, 16)) + (WS_RL(v, 32) + WS_RL(v, 48)); }
; __device__ __forceinline__ void phase_normmod_bf(const bf16* hin, const float* g, const float* shift, const float* scale  , bf16* U, int gw, int NGW, int lane) {
;     ...
;             for (int j = 0; j < 8; ++j) ss += (v[j].x * v[j].x + v[j].y * v[j].y) + (v[j].z * v[j].z + v[j].w * v[j].w);
;             const float rstd = 1.0f / sqrtf(wave_sum(ss) * (1.0f / DM) + EPS);
;             GAS v4u* o16 = (GAS v4u*)(U + (size_t)(r0 + rr) * DM) + lane;
; #pragma unroll
;             for (int j = 0; j < 4; ++j) { const f32x4 y0 = v[2 * j] * rstd * mul[2 * j] + add[2 * j], y1 = v[2 * j + 1] * rstd * mul[2 * j + 1] + add[2 * j + 1];
;                 v4u w; w.x = pk2(y0.x, y0.y); w.y = pk2(y0.z, y0.w); w.z = pk2(y1.x, y1.y); w.w = pk2(y1.z, y1.w); o16[64 * j] = w; }
	v_lshlrev_b32_e32 v88, 16, v124
	v_pk_add_f32 v[100:101], v[100:101], v[104:105]
	v_and_b32_e32 v105, 0xffff0000, v119
	v_and_b32_e32 v104, 0xffff0000, v118
	v_pk_add_f32 v[114:115], v[100:101], v[100:101] op_sel_hi:[0,1]
	v_lshlrev_b32_e32 v101, 16, v119
	v_lshlrev_b32_e32 v100, 16, v118
	v_pk_mul_f32 v[116:117], v[104:105], v[104:105]
	v_lshlrev_b32_e32 v118, 16, v121
	v_and_b32_e32 v35, 0xffff0000, v124
	v_lshlrev_b32_e32 v90, 16, v125
	v_and_b32_e32 v91, 0xffff0000, v125
	v_pk_fma_f32 v[116:117], v[100:101], v[100:101], v[116:117]
	v_mul_f32_e32 v95, v98, v98
	v_mul_f32_e32 v125, v99, v99
	v_and_b32_e32 v119, 0xffff0000, v121
	v_mul_f32_e32 v0, v118, v118
	v_mov_b32_e32 v124, v94
	v_pk_add_f32 v[116:117], v[116:117], v[116:117] op_sel_hi:[0,1]
	v_pk_fma_f32 v[126:127], v[118:119], v[118:119], v[0:1] op_sel_hi:[1,1,0]
	v_pk_add_f32 v[124:125], v[94:95], v[124:125]
	v_mul_f32_e32 v126, v120, v120
	v_mul_f32_e32 v114, v96, v96
	v_mul_f32_e32 v116, v97, v97
	v_mul_f32_e32 v128, v94, v94
	v_mov_b32_e32 v129, v125
	v_pk_add_f32 v[124:125], v[128:129], v[126:127]
	v_pk_add_f32 v[114:115], v[114:115], v[116:117]
	v_and_b32_e32 v117, 0xffff0000, v109
	v_pk_add_f32 v[114:115], v[124:125], v[114:115]
	v_and_b32_e32 v116, 0xffff0000, v108
	v_pk_add_f32 v[124:125], v[114:115], v[114:115] op_sel_hi:[0,1]
	v_lshlrev_b32_e32 v115, 16, v109
	v_lshlrev_b32_e32 v114, 16, v108
	v_pk_mul_f32 v[108:109], v[116:117], v[116:117]
	v_lshlrev_b32_e32 v92, 16, v122
	v_pk_fma_f32 v[108:109], v[114:115], v[114:115], v[108:109]
	v_and_b32_e32 v93, 0xffff0000, v122
	v_pk_add_f32 v[126:127], v[108:109], v[108:109] op_sel_hi:[0,1]
	v_lshlrev_b32_e32 v108, 16, v123
	v_mul_f32_e32 v89, v92, v92
	v_mul_f32_e32 v129, v93, v93
	v_and_b32_e32 v109, 0xffff0000, v123
	v_mul_f32_e32 v0, v108, v108
	v_mov_b32_e32 v128, v88
	v_pk_fma_f32 v[122:123], v[108:109], v[108:109], v[0:1] op_sel_hi:[1,1,0]
	v_pk_add_f32 v[128:129], v[88:89], v[128:129]
	v_mul_f32_e32 v122, v35, v35
	v_mul_f32_e32 v126, v90, v90
	v_mul_f32_e32 v124, v91, v91
	v_mul_f32_e32 v130, v88, v88
	v_mov_b32_e32 v131, v129
	v_pk_add_f32 v[122:123], v[130:131], v[122:123]
	v_pk_add_f32 v[124:125], v[126:127], v[124:125]
	v_mov_b32_e32 v127, v112
	v_pk_add_f32 v[122:123], v[122:123], v[124:125]
	v_mov_b32_e32 v125, v106
	v_add_f32_e32 v0, v122, v123
	v_mov_b32_e32 v106, v103
	v_mov_b32_e32 v124, v102
	v_add_f32_dpp v0, v0, v0 quad_perm:[1,0,3,2] row_mask:0xf bank_mask:0xf bound_ctrl:1
	v_mov_b32_e32 v112, v111
	v_mov_b32_e32 v126, v110
	v_add_f32_dpp v0, v0, v0 quad_perm:[2,3,0,1] row_mask:0xf bank_mask:0xf bound_ctrl:1
	s_nop 1
	v_add_f32_dpp v0, v0, v0 row_half_mirror row_mask:0xf bank_mask:0xf bound_ctrl:1
	s_nop 1
	v_add_f32_dpp v0, v0, v0 row_mirror row_mask:0xf bank_mask:0xf bound_ctrl:1
	s_nop 0
	v_readlane_b32 s15, v0, 16
	v_readlane_b32 s16, v0, 48
	v_readlane_b32 s12, v0, 0
	v_readlane_b32 s13, v0, 32
	v_mov_b32_e32 v122, s15
	v_mov_b32_e32 v123, s16
	v_pk_add_f32 v[122:123], s[12:13], v[122:123]
	s_nop 0
	v_add_f32_e32 v0, v122, v123
	v_fmamk_f32 v0, v0, 0x3a000000, v192
	v_rsq_f32_e32 v89, v0
	s_nop 0
	v_mul_f32_e32 v95, v0, v89
	v_fma_f32 v95, -v95, v89, 1.0
	v_mul_f32_e32 v121, 0.5, v89
	v_fma_f32 v0, v121, v95, v89
	v_pk_mul_f32 v[102:103], v[106:107], v[0:1] op_sel_hi:[1,0]
	v_pk_mul_f32 v[106:107], v[112:113], v[0:1] op_sel_hi:[1,0]
	v_pk_fma_f32 v[102:103], v[62:63], v[102:103], v[2:3]
	v_pk_fma_f32 v[106:107], v[60:61], v[106:107], v[4:5]
	v_cvt_pk_bf16_f32 v112, v102, v103
	v_mov_b32_e32 v102, v100
	v_mov_b32_e32 v103, v104
	v_mov_b32_e32 v104, v101
	v_pk_mul_f32 v[102:103], v[0:1], v[102:103] op_sel_hi:[0,1]
	v_pk_mul_f32 v[100:101], v[0:1], v[104:105] op_sel_hi:[0,1]
	v_pk_mul_f32 v[98:99], v[98:99], v[0:1] op_sel_hi:[1,0]
	v_pk_mul_f32 v[104:105], v[118:119], v[0:1] op_sel_hi:[1,0]
	v_cvt_pk_bf16_f32 v113, v106, v107
	v_pk_fma_f32 v[100:101], v[64:65], v[100:101], v[16:17]
	v_pk_fma_f32 v[102:103], v[66:67], v[102:103], v[14:15]
	v_pk_fma_f32 v[104:105], v[68:69], v[104:105], v[12:13]
	v_pk_fma_f32 v[106:107], v[70:71], v[98:99], v[10:11]
	v_lshl_add_u64 v[122:123], v[48:49], 0, s[8:9]
	v_cvt_pk_bf16_f32 v98, v102, v103
	v_cvt_pk_bf16_f32 v99, v100, v101
	v_cvt_pk_bf16_f32 v100, v106, v107
	v_cvt_pk_bf16_f32 v101, v104, v105
	global_store_dwordx4 v[122:123], v[98:101], off offset:-1024
	v_mov_b32_e32 v95, v120
	v_pk_mul_f32 v[94:95], v[94:95], v[0:1] op_sel_hi:[1,0]
	v_mov_b32_e32 v98, v114
	v_mov_b32_e32 v99, v116
	v_mov_b32_e32 v116, v115
	v_pk_mul_f32 v[96:97], v[96:97], v[0:1] op_sel_hi:[1,0]
	v_pk_mul_f32 v[98:99], v[0:1], v[98:99] op_sel_hi:[0,1]
	v_pk_mul_f32 v[100:101], v[0:1], v[116:117] op_sel_hi:[0,1]
	v_pk_fma_f32 v[96:97], v[80:81], v[96:97], v[24:25]
	v_pk_fma_f32 v[94:95], v[82:83], v[94:95], v[22:23]
	v_pk_fma_f32 v[100:101], v[72:73], v[100:101], v[20:21]
	v_pk_fma_f32 v[98:99], v[74:75], v[98:99], v[18:19]
	v_cvt_pk_bf16_f32 v94, v94, v95
	v_cvt_pk_bf16_f32 v95, v96, v97
	v_cvt_pk_bf16_f32 v96, v98, v99
	v_cvt_pk_bf16_f32 v97, v100, v101
	v_mov_b32_e32 v89, v35
	v_pk_mul_f32 v[124:125], v[124:125], v[0:1] op_sel_hi:[1,0]
	v_pk_mul_f32 v[126:127], v[126:127], v[0:1] op_sel_hi:[1,0]
	global_store_dwordx4 v[122:123], v[94:97], off
	v_pk_mul_f32 v[92:93], v[92:93], v[0:1] op_sel_hi:[1,0]
	v_pk_mul_f32 v[88:89], v[88:89], v[0:1] op_sel_hi:[1,0]
	v_pk_mul_f32 v[94:95], v[108:109], v[0:1] op_sel_hi:[1,0]
	v_pk_mul_f32 v[90:91], v[90:91], v[0:1] op_sel_hi:[1,0]
	s_add_u32 s8, s8, 0x1000
	v_pk_fma_f32 v[126:127], v[56:57], v[126:127], v[8:9]
	v_pk_fma_f32 v[124:125], v[58:59], v[124:125], v[6:7]
	v_pk_fma_f32 v[94:95], v[84:85], v[94:95], v[28:29]
	v_pk_fma_f32 v[92:93], v[86:87], v[92:93], v[26:27]
	v_pk_fma_f32 v[96:97], v[76:77], v[90:91], v[32:33]
	v_pk_fma_f32 v[90:91], v[78:79], v[88:89], v[30:31]
	s_addc_u32 s9, s9, 0
	v_cvt_pk_bf16_f32 v110, v124, v125
	v_cvt_pk_bf16_f32 v111, v126, v127
	v_cvt_pk_bf16_f32 v88, v92, v93
	v_cvt_pk_bf16_f32 v89, v94, v95
	v_cvt_pk_bf16_f32 v90, v90, v91
	v_cvt_pk_bf16_f32 v91, v96, v97
	s_cmpk_eq_u32 s8, 0x8000
	global_store_dwordx4 v[122:123], v[110:113], off offset:-2048
	global_store_dwordx4 v[122:123], v[88:91], off offset:1024
	s_cbranch_scc0 .LBB0_232
	s_add_i32 s14, s14, s88
	v_lshl_add_u64 v[46:47], v[46:47], 0, s[20:21]
	s_cmpk_gt_i32 s14, 0x3fff
	v_lshl_add_u64 v[48:49], v[48:49], 0, s[20:21]
	s_cbranch_scc0 .LBB0_231

; #define GAS __attribute__((address_space(1)))
; __device__ __forceinline__ unsigned pk2(float lo, float hi) { const pk_f2 v = {lo, hi}; return __builtin_bit_cast(unsigned, __builtin_convertvector(v, pk_b2)); }
; __device__ __forceinline__ float wave_sum(float v) { v = row16_sum(v); return (WS_RL(v, 0) + WS_RL(v, 16)) + (WS_RL(v, 32) + WS_RL(v, 48)); }
; __device__ __forceinline__ void phase_normmod(const float* hin, const float* g, const float* shift, const float* scale  , bf16* U, int gw, int NGW, int lane) {
;     ...
;         for (int rr = 0; rr < 8; ++rr) {
;             const GAS f32x4* xr = (const GAS f32x4*)(hin + (size_t)(r0 + rr) * DM) + lane;
;             f32x4 v[8]; float ss = 0.f;
; #pragma unroll
;             for (int j = 0; j < 8; ++j) { v[j] = xr[64 * j]; ss += (v[j].x * v[j].x + v[j].y * v[j].y) + (v[j].z * v[j].z + v[j].w * v[j].w); }
;             const float rstd = 1.0f / sqrtf(wave_sum(ss) * (1.0f / DM) + EPS);
;             GAS v2u* o8 = (GAS v2u*)(U + (size_t)(r0 + rr) * DM) + lane;
; #pragma unroll
;             for (int j = 0; j < 8; ++j) { const f32x4 y = v[j] * rstd * mul[j] + add[j]; v2u w; w.x = pk2(y.x, y.y); w.y = pk2(y.z, y.w); o8[64 * j] = w; }
;         }
.LBB0_239:
	v_lshl_add_u64 v[102:103], v[50:51], 0, s[0:1]
	global_load_dwordx4 v[86:89], v[102:103], off
	global_load_dwordx4 v[90:93], v[102:103], off offset:1024
	v_add_co_u32_e32 v114, vcc, s8, v102
	s_add_u32 s0, s0, 0x2000
	s_nop 0
	v_addc_co_u32_e32 v115, vcc, 0, v103, vcc
	s_addc_u32 s1, s1, 0
	s_cmp_eq_u32 s0, 0x10000
	s_waitcnt vmcnt(1)
	v_mov_b32_e32 v96, v87
	s_waitcnt vmcnt(0)
	v_mov_b32_e32 v97, v91
	v_mov_b32_e32 v94, v86
	v_mov_b32_e32 v95, v90
	v_pk_mul_f32 v[96:97], v[96:97], v[96:97]
	v_mov_b32_e32 v98, v89
	v_mov_b32_e32 v99, v93
	v_pk_fma_f32 v[94:95], v[94:95], v[94:95], v[96:97]
	v_mov_b32_e32 v96, v88
	v_mov_b32_e32 v97, v92
	v_pk_mul_f32 v[98:99], v[98:99], v[98:99]
	s_nop 0
	v_pk_fma_f32 v[96:97], v[96:97], v[96:97], v[98:99]
	s_nop 0
	v_pk_add_f32 v[106:107], v[94:95], v[96:97]
	global_load_dwordx4 v[94:97], v[102:103], off offset:2048
	v_pk_add_f32 v[106:107], v[106:107], v[106:107] op_sel:[0,1] op_sel_hi:[1,0]
	s_waitcnt vmcnt(0)
	v_pk_mul_f32 v[98:99], v[96:97], v[96:97]
	v_pk_mul_f32 v[100:101], v[94:95], v[94:95]
	s_nop 0
	v_pk_mov_b32 v[104:105], v[100:101], v[98:99] op_sel:[1,0]
	v_mov_b32_e32 v101, v99
	v_pk_add_f32 v[108:109], v[104:105], v[100:101]
	global_load_dwordx4 v[98:101], v[102:103], off offset:3072
	v_pk_add_f32 v[108:109], v[108:109], v[108:109] op_sel:[0,1] op_sel_hi:[1,0]
	global_load_dwordx4 v[102:105], v[114:115], off
	s_waitcnt vmcnt(0)
	v_mul_f32_e32 v0, v102, v102
	v_mul_f32_e32 v110, v103, v103
	v_mov_b32_e32 v107, v0
	v_mov_b32_e32 v109, v110
	v_mul_f32_e32 v0, v99, v99
	v_mul_f32_e32 v111, v104, v104
	v_pk_add_f32 v[106:107], v[106:107], v[108:109]
	v_pk_fma_f32 v[108:109], v[98:99], v[98:99], v[0:1] op_sel_hi:[1,1,0]
	v_mul_f32_e32 v0, v101, v101
	v_mul_f32_e32 v112, v105, v105
	v_mov_b32_e32 v109, v111
	v_pk_fma_f32 v[110:111], v[100:101], v[100:101], v[0:1] op_sel_hi:[1,1,0]
	s_nop 0
	v_mov_b32_e32 v111, v112
	v_pk_add_f32 v[108:109], v[108:109], v[110:111]
	s_nop 0
	v_pk_add_f32 v[118:119], v[106:107], v[108:109]
	global_load_dwordx4 v[106:109], v[114:115], off offset:1024
	v_pk_add_f32 v[118:119], v[118:119], v[118:119] op_sel:[0,1] op_sel_hi:[1,0]
	s_waitcnt vmcnt(0)
	v_pk_mul_f32 v[110:111], v[108:109], v[108:109]
	v_pk_mul_f32 v[112:113], v[106:107], v[106:107]
	s_nop 0
	v_pk_mov_b32 v[116:117], v[112:113], v[110:111] op_sel:[1,0]
	v_mov_b32_e32 v113, v111
	v_pk_add_f32 v[120:121], v[116:117], v[112:113]
	global_load_dwordx4 v[110:113], v[114:115], off offset:2048
	s_nop 0
	global_load_dwordx4 v[114:117], v[114:115], off offset:3072
	v_pk_add_f32 v[120:121], v[120:121], v[120:121] op_sel:[0,1] op_sel_hi:[1,0]
	s_waitcnt vmcnt(0)
	v_mul_f32_e32 v0, v114, v114
	v_mul_f32_e32 v122, v115, v115
	v_mov_b32_e32 v119, v0
	v_mov_b32_e32 v121, v122
	v_mul_f32_e32 v0, v111, v111
	v_mul_f32_e32 v123, v116, v116
	v_pk_add_f32 v[118:119], v[118:119], v[120:121]
	v_pk_fma_f32 v[120:121], v[110:111], v[110:111], v[0:1] op_sel_hi:[1,1,0]
	v_mul_f32_e32 v0, v113, v113
	v_mul_f32_e32 v124, v117, v117
	v_mov_b32_e32 v121, v123
	v_pk_fma_f32 v[122:123], v[112:113], v[112:113], v[0:1] op_sel_hi:[1,1,0]
	s_nop 0
	v_mov_b32_e32 v123, v124
	v_pk_add_f32 v[120:121], v[120:121], v[122:123]
	s_nop 0
	v_pk_add_f32 v[118:119], v[118:119], v[120:121]
	s_nop 0
	v_add_f32_e32 v0, v118, v119
	s_nop 1
	v_add_f32_dpp v0, v0, v0 quad_perm:[1,0,3,2] row_mask:0xf bank_mask:0xf bound_ctrl:1
	s_nop 1
	v_add_f32_dpp v0, v0, v0 quad_perm:[2,3,0,1] row_mask:0xf bank_mask:0xf bound_ctrl:1
	s_nop 1
	v_add_f32_dpp v0, v0, v0 row_half_mirror row_mask:0xf bank_mask:0xf bound_ctrl:1
	s_nop 1
	v_add_f32_dpp v0, v0, v0 row_mirror row_mask:0xf bank_mask:0xf bound_ctrl:1
	s_nop 0
	v_readlane_b32 s3, v0, 16
	v_readlane_b32 s7, v0, 48
	v_readlane_b32 s4, v0, 0
	v_readlane_b32 s5, v0, 32
	v_mov_b32_e32 v118, s3
	v_mov_b32_e32 v119, s7
	v_pk_add_f32 v[118:119], s[4:5], v[118:119]
	s_nop 0
	v_add_f32_e32 v0, v118, v119
	v_fmamk_f32 v0, v0, 0x3a000000, v192
	v_rsq_f32_e32 v118, v0
	s_nop 0
	v_mul_f32_e32 v119, v0, v118
	v_fma_f32 v119, -v119, v118, 1.0
	v_mul_f32_e32 v120, 0.5, v118
	v_fma_f32 v0, v120, v119, v118
	v_pk_mul_f32 v[86:87], v[86:87], v[0:1] op_sel_hi:[1,0]
	v_pk_mul_f32 v[88:89], v[88:89], v[0:1] op_sel_hi:[1,0]
	v_pk_fma_f32 v[86:87], v[54:55], v[86:87], v[2:3]
	v_pk_fma_f32 v[88:89], v[52:53], v[88:89], v[4:5]
	v_cvt_pk_bf16_f32 v86, v86, v87
	v_cvt_pk_bf16_f32 v87, v88, v89
	global_store_dwordx2 v[84:85], v[86:87], off offset:-2048
	v_pk_mul_f32 v[86:87], v[90:91], v[0:1] op_sel_hi:[1,0]
	v_pk_mul_f32 v[88:89], v[92:93], v[0:1] op_sel_hi:[1,0]
	v_pk_fma_f32 v[86:87], v[58:59], v[86:87], v[6:7]
	v_pk_fma_f32 v[88:89], v[56:57], v[88:89], v[8:9]
	v_cvt_pk_bf16_f32 v86, v86, v87
	v_cvt_pk_bf16_f32 v87, v88, v89
	global_store_dwordx2 v[84:85], v[86:87], off offset:-1536
	v_pk_mul_f32 v[86:87], v[94:95], v[0:1] op_sel_hi:[1,0]
	v_pk_mul_f32 v[88:89], v[96:97], v[0:1] op_sel_hi:[1,0]
	v_pk_fma_f32 v[86:87], v[62:63], v[86:87], v[10:11]
	v_pk_fma_f32 v[88:89], v[60:61], v[88:89], v[12:13]
	v_cvt_pk_bf16_f32 v86, v86, v87
	v_cvt_pk_bf16_f32 v87, v88, v89
	global_store_dwordx2 v[84:85], v[86:87], off offset:-1024
	v_pk_mul_f32 v[86:87], v[98:99], v[0:1] op_sel_hi:[1,0]
	v_pk_mul_f32 v[88:89], v[100:101], v[0:1] op_sel_hi:[1,0]
	v_pk_fma_f32 v[86:87], v[66:67], v[86:87], v[14:15]
	v_pk_fma_f32 v[88:89], v[64:65], v[88:89], v[16:17]
	v_cvt_pk_bf16_f32 v86, v86, v87
	v_cvt_pk_bf16_f32 v87, v88, v89
	global_store_dwordx2 v[84:85], v[86:87], off offset:-512
	v_pk_mul_f32 v[86:87], v[102:103], v[0:1] op_sel_hi:[1,0]
	v_pk_mul_f32 v[88:89], v[104:105], v[0:1] op_sel_hi:[1,0]
	v_pk_fma_f32 v[86:87], v[70:71], v[86:87], v[18:19]
	v_pk_fma_f32 v[88:89], v[68:69], v[88:89], v[20:21]
	v_cvt_pk_bf16_f32 v86, v86, v87
	v_cvt_pk_bf16_f32 v87, v88, v89
	global_store_dwordx2 v[84:85], v[86:87], off
	v_pk_mul_f32 v[86:87], v[106:107], v[0:1] op_sel_hi:[1,0]
	v_pk_mul_f32 v[88:89], v[108:109], v[0:1] op_sel_hi:[1,0]
	v_pk_fma_f32 v[86:87], v[74:75], v[86:87], v[22:23]
	v_pk_fma_f32 v[88:89], v[72:73], v[88:89], v[24:25]
	v_cvt_pk_bf16_f32 v86, v86, v87
	v_cvt_pk_bf16_f32 v87, v88, v89
	global_store_dwordx2 v[84:85], v[86:87], off offset:512
	v_pk_mul_f32 v[86:87], v[110:111], v[0:1] op_sel_hi:[1,0]
	v_pk_mul_f32 v[88:89], v[112:113], v[0:1] op_sel_hi:[1,0]
	v_pk_fma_f32 v[86:87], v[78:79], v[86:87], v[26:27]
	v_pk_fma_f32 v[88:89], v[76:77], v[88:89], v[28:29]
	v_cvt_pk_bf16_f32 v86, v86, v87
	v_cvt_pk_bf16_f32 v87, v88, v89
	global_store_dwordx2 v[84:85], v[86:87], off offset:1024
	v_pk_mul_f32 v[86:87], v[114:115], v[0:1] op_sel_hi:[1,0]
	v_pk_mul_f32 v[88:89], v[116:117], v[0:1] op_sel_hi:[1,0]
	v_pk_fma_f32 v[86:87], v[82:83], v[86:87], v[30:31]
	v_pk_fma_f32 v[88:89], v[80:81], v[88:89], v[32:33]
	v_cvt_pk_bf16_f32 v86, v86, v87
	v_cvt_pk_bf16_f32 v87, v88, v89
	global_store_dwordx2 v[84:85], v[86:87], off offset:1536
	v_lshl_add_u64 v[84:85], v[84:85], 0, s[12:13]
	s_cbranch_scc0 .LBB0_239
; __device__ __forceinline__ void phase_normmod(const float* hin, const float* g, const float* shift, const float* scale  , bf16* U, int gw, int NGW, int lane) {
;     for (int r0 = gw * 8; r0 < M; r0 += NGW * 8) {
	s_add_i32 s2, s2, s88
	v_lshl_add_u64 v[50:51], v[50:51], 0, s[24:25]
	s_cmpk_gt_i32 s2, 0x3fff
	v_lshl_add_u64 v[34:35], v[34:35], 0, s[20:21]
	s_cbranch_scc0 .LBB0_238

; #define PM_LDH(voff, soff) __builtin_amdgcn_raw_buffer_load_b128(rsH, (voff), (soff), 0)
; #define PM_UNPK(q_, f_) do { f_[0] = bflo(q_.x); f_[1] = bfhi(q_.x); f_[2] = bflo(q_.y); f_[3] = bfhi(q_.y); f_[4] = bflo(q_.z); f_[5] = bfhi(q_.z); f_[6] = bflo(q_.w); f_[7] = bfhi(q_.w); } while (0)
; template <bool XF32> ...
;     ...
;         else for (int rp = wave; 2 * rp < 64 + halo; rp += 2 * NWAVES) {
;             int rrq[2]; float ssq[2]; v4u qq[2][XF32 ? 16 : 8];
; #pragma unroll
;             for (int z = 0; z < 2; ++z) { const int rr = 2 * (rp + NWAVES * z) + h5, rrc = rr < 64 + halo ? rr : 63 + halo, row = r0 - halo + rrc; rrq[z] = rr;
;                 const unsigned vo = (unsigned)row * (DM * ES) + (unsigned)l31 * 16u;
; #pragma unroll
;                 for (int j = 0; j < (XF32 ? 16 : 8); ++j) qq[z][j] = PM_LDH(vo, (unsigned)j * 512u); }
; #pragma unroll
;             for (int z = 0; z < 2; ++z) { float ss = 0.f;
; #pragma unroll
;                 for (int j = 0; j < (XF32 ? 16 : 8); ++j) { const v4u q = qq[z][j];
;                     if constexpr (XF32) { const f32x4 v = __builtin_bit_cast(f32x4, q); ss += (v.x * v.x + v.y * v.y) + (v.z * v.z + v.w * v.w); }
;                     else { float f[8]; PM_UNPK(q, f); ss += ((f[0] * f[0] + f[1] * f[1]) + (f[2] * f[2] + f[3] * f[3])) + ((f[4] * f[4] + f[5] * f[5]) + (f[6] * f[6] + f[7] * f[7])); } }
.LBB0_430:
	s_nop 0
	v_add_u32_e32 v2, s15, v203
	v_cmp_le_i32_e32 vcc, s2, v2
	v_mov_b32_e32 v3, s3
	s_movk_i32 s16, 0x400
	v_cndmask_b32_e32 v4, v2, v3, vcc
	v_add_u32_e32 v4, s14, v4
	v_lshl_or_b32 v4, v4, 12, v204
	buffer_load_dwordx4 v[56:59], v4, s[4:7], 0 offen
	buffer_load_dwordx4 v[60:63], v4, s[4:7], s39 offen
	buffer_load_dwordx4 v[64:67], v4, s[4:7], s16 offen
	s_movk_i32 s20, 0x600
	buffer_load_dwordx4 v[50:53], v4, s[4:7], s20 offen
	buffer_load_dwordx4 v[46:49], v4, s[4:7], s38 offen
	s_movk_i32 s22, 0xa00
	buffer_load_dwordx4 v[42:45], v4, s[4:7], s22 offen
	s_movk_i32 s21, 0xc00
	buffer_load_dwordx4 v[38:41], v4, s[4:7], s21 offen
	s_movk_i32 s23, 0xe00
	buffer_load_dwordx4 v[34:37], v4, s[4:7], s23 offen
	v_add_u32_e32 v2, 16, v2
	v_cmp_le_i32_e64 s[44:45], s2, v2
	s_nor_b64 s[26:27], s[36:37], vcc
	s_waitcnt vmcnt(7)
	v_lshlrev_b32_e32 v55, 16, v56
	v_cndmask_b32_e64 v2, v2, v3, s[44:45]
	v_add_u32_e32 v2, s14, v2
	v_lshl_or_b32 v2, v2, 12, v204
	buffer_load_dwordx4 v[30:33], v2, s[4:7], 0 offen
	buffer_load_dwordx4 v[26:29], v2, s[4:7], s39 offen
	buffer_load_dwordx4 v[22:25], v2, s[4:7], s16 offen
	buffer_load_dwordx4 v[18:21], v2, s[4:7], s20 offen
	buffer_load_dwordx4 v[14:17], v2, s[4:7], s38 offen
	buffer_load_dwordx4 v[10:13], v2, s[4:7], s22 offen
	buffer_load_dwordx4 v[6:9], v2, s[4:7], s21 offen
	s_nop 0
	buffer_load_dwordx4 v[2:5], v2, s[4:7], s23 offen
	v_and_b32_e32 v56, 0xffff0000, v56
	v_lshlrev_b32_e32 v68, 16, v57
	v_and_b32_e32 v57, 0xffff0000, v57
	v_mul_f32_e32 v56, v56, v56
	v_fmac_f32_e32 v56, v55, v55
	v_mul_f32_e32 v55, v57, v57
	v_lshlrev_b32_e32 v69, 16, v58
	v_and_b32_e32 v58, 0xffff0000, v58
	v_lshlrev_b32_e32 v70, 16, v59
	v_and_b32_e32 v59, 0xffff0000, v59
	v_fmac_f32_e32 v55, v68, v68
	v_add_f32_e32 v55, v56, v55
	v_mul_f32_e32 v56, v58, v58
	v_mul_f32_e32 v57, v59, v59
	v_fmac_f32_e32 v56, v69, v69
	v_fmac_f32_e32 v57, v70, v70
	v_add_f32_e32 v56, v56, v57
	s_waitcnt vmcnt(14)
	v_and_b32_e32 v57, 0xffff0000, v60
	v_add_f32_e32 v55, v55, v56
	v_lshlrev_b32_e32 v56, 16, v60
	v_and_b32_e32 v59, 0xffff0000, v61
	v_mul_f32_e32 v57, v57, v57
	v_lshlrev_b32_e32 v58, 16, v61
	v_fmac_f32_e32 v57, v56, v56
	v_mul_f32_e32 v56, v59, v59
	v_lshlrev_b32_e32 v60, 16, v62
	v_and_b32_e32 v61, 0xffff0000, v62
	v_lshlrev_b32_e32 v62, 16, v63
	v_and_b32_e32 v63, 0xffff0000, v63
	v_fmac_f32_e32 v56, v58, v58
	v_add_f32_e32 v56, v57, v56
	v_mul_f32_e32 v57, v61, v61
	v_mul_f32_e32 v58, v63, v63
	v_fmac_f32_e32 v57, v60, v60
	v_fmac_f32_e32 v58, v62, v62
	v_add_f32_e32 v57, v57, v58
	v_add_f32_e32 v56, v56, v57
	s_waitcnt vmcnt(13)
	v_and_b32_e32 v57, 0xffff0000, v64
	v_add_f32_e32 v55, v55, v56
	v_lshlrev_b32_e32 v56, 16, v64
	v_and_b32_e32 v59, 0xffff0000, v65
	v_mul_f32_e32 v57, v57, v57
	v_lshlrev_b32_e32 v58, 16, v65
	v_fmac_f32_e32 v57, v56, v56
	v_mul_f32_e32 v56, v59, v59
	v_and_b32_e32 v61, 0xffff0000, v66
	v_and_b32_e32 v63, 0xffff0000, v67
	v_fmac_f32_e32 v56, v58, v58
	v_lshlrev_b32_e32 v60, 16, v66
	v_lshlrev_b32_e32 v62, 16, v67
	v_add_f32_e32 v56, v57, v56
	v_mul_f32_e32 v57, v61, v61
	v_mul_f32_e32 v58, v63, v63
	v_fmac_f32_e32 v57, v60, v60
	v_fmac_f32_e32 v58, v62, v62
	v_add_f32_e32 v57, v57, v58
	v_add_f32_e32 v56, v56, v57
	v_add_f32_e32 v55, v55, v56
	s_waitcnt vmcnt(12)
	v_lshlrev_b32_e32 v56, 16, v50
	v_and_b32_e32 v50, 0xffff0000, v50
	v_lshlrev_b32_e32 v57, 16, v51
	v_and_b32_e32 v51, 0xffff0000, v51
	v_mul_f32_e32 v50, v50, v50
	v_mul_f32_e32 v51, v51, v51
	v_lshlrev_b32_e32 v58, 16, v52
	v_and_b32_e32 v52, 0xffff0000, v52
	v_lshlrev_b32_e32 v59, 16, v53
	v_and_b32_e32 v53, 0xffff0000, v53
	v_fmac_f32_e32 v50, v56, v56
	v_fmac_f32_e32 v51, v57, v57
	v_add_f32_e32 v50, v50, v51
	v_mul_f32_e32 v51, v52, v52
	v_mul_f32_e32 v52, v53, v53
	v_fmac_f32_e32 v51, v58, v58
	v_fmac_f32_e32 v52, v59, v59
	v_add_f32_e32 v51, v51, v52
	v_add_f32_e32 v50, v50, v51
	s_waitcnt vmcnt(11)
	v_lshlrev_b32_e32 v51, 16, v46
	v_and_b32_e32 v46, 0xffff0000, v46
	v_lshlrev_b32_e32 v52, 16, v47
	v_and_b32_e32 v47, 0xffff0000, v47
	v_mul_f32_e32 v46, v46, v46
	v_mul_f32_e32 v47, v47, v47
	v_add_f32_e32 v50, v55, v50
	v_lshlrev_b32_e32 v53, 16, v48
	v_and_b32_e32 v48, 0xffff0000, v48
	v_lshlrev_b32_e32 v55, 16, v49
	v_and_b32_e32 v49, 0xffff0000, v49
	v_fmac_f32_e32 v46, v51, v51
	v_fmac_f32_e32 v47, v52, v52
	v_add_f32_e32 v46, v46, v47
	v_mul_f32_e32 v47, v48, v48
	v_mul_f32_e32 v48, v49, v49
	v_fmac_f32_e32 v47, v53, v53
	v_fmac_f32_e32 v48, v55, v55
	v_add_f32_e32 v47, v47, v48
	v_add_f32_e32 v46, v46, v47
	s_waitcnt vmcnt(10)
	v_lshlrev_b32_e32 v47, 16, v42
	v_and_b32_e32 v42, 0xffff0000, v42
	v_lshlrev_b32_e32 v48, 16, v43
	v_and_b32_e32 v43, 0xffff0000, v43
	v_mul_f32_e32 v42, v42, v42
	v_mul_f32_e32 v43, v43, v43
	v_add_f32_e32 v46, v50, v46
	v_lshlrev_b32_e32 v49, 16, v44
	v_and_b32_e32 v44, 0xffff0000, v44
	v_lshlrev_b32_e32 v50, 16, v45
	v_and_b32_e32 v45, 0xffff0000, v45
	v_fmac_f32_e32 v42, v47, v47
	v_fmac_f32_e32 v43, v48, v48
	v_add_f32_e32 v42, v42, v43
	v_mul_f32_e32 v43, v44, v44
	v_mul_f32_e32 v44, v45, v45
	v_fmac_f32_e32 v43, v49, v49
	v_fmac_f32_e32 v44, v50, v50
	v_add_f32_e32 v43, v43, v44
	v_add_f32_e32 v42, v42, v43
	s_waitcnt vmcnt(9)
	v_lshlrev_b32_e32 v43, 16, v38
	v_and_b32_e32 v38, 0xffff0000, v38
	v_lshlrev_b32_e32 v44, 16, v39
	v_and_b32_e32 v39, 0xffff0000, v39
	v_mul_f32_e32 v38, v38, v38
	v_mul_f32_e32 v39, v39, v39
	v_add_f32_e32 v42, v46, v42
	v_lshlrev_b32_e32 v45, 16, v40
	v_and_b32_e32 v40, 0xffff0000, v40
	v_lshlrev_b32_e32 v46, 16, v41
	v_and_b32_e32 v41, 0xffff0000, v41
	v_fmac_f32_e32 v38, v43, v43
	v_fmac_f32_e32 v39, v44, v44
	v_add_f32_e32 v38, v38, v39
	v_mul_f32_e32 v39, v40, v40
	v_mul_f32_e32 v40, v41, v41
	v_fmac_f32_e32 v39, v45, v45
	v_fmac_f32_e32 v40, v46, v46
	v_add_f32_e32 v39, v39, v40
	v_add_f32_e32 v38, v38, v39
	s_waitcnt vmcnt(8)
; #define PM_UNPK(q_, f_) do { f_[0] = bflo(q_.x); f_[1] = bfhi(q_.x); f_[2] = bflo(q_.y); f_[3] = bfhi(q_.y); f_[4] = bflo(q_.z); f_[5] = bfhi(q_.z); f_[6] = bflo(q_.w); f_[7] = bfhi(q_.w); } while (0)
; template <bool XF32> ...
;     ...
;                     else { float f[8]; PM_UNPK(q, f); ss += ((f[0] * f[0] + f[1] * f[1]) + (f[2] * f[2] + f[3] * f[3])) + ((f[4] * f[4] + f[5] * f[5]) + (f[6] * f[6] + f[7] * f[7])); } }
;                 ssq[z] = ss; }
; #pragma unroll
;             for (int z = 0; z < 2; ++z) { float ss = ssq[z];
;                 ss = half_sum(ss);
;                 const float rstd = 1.0f / sqrtf(ss * (1.0f / DM) + EPS);
;                 if (l31 == 0 && rrq[z] < 64 + halo) rstdL[rrq[z] + 15 - halo] = rstd; }
	v_lshlrev_b32_e32 v39, 16, v34
	v_and_b32_e32 v34, 0xffff0000, v34
	v_lshlrev_b32_e32 v40, 16, v35
	v_and_b32_e32 v35, 0xffff0000, v35
	v_mul_f32_e32 v34, v34, v34
	v_mul_f32_e32 v35, v35, v35
	v_add_f32_e32 v38, v42, v38
	v_lshlrev_b32_e32 v41, 16, v36
	v_and_b32_e32 v36, 0xffff0000, v36
	v_lshlrev_b32_e32 v42, 16, v37
	v_and_b32_e32 v37, 0xffff0000, v37
	v_fmac_f32_e32 v34, v39, v39
	v_fmac_f32_e32 v35, v40, v40
	v_add_f32_e32 v34, v34, v35
	v_mul_f32_e32 v35, v36, v36
	v_mul_f32_e32 v36, v37, v37
	v_fmac_f32_e32 v35, v41, v41
	v_fmac_f32_e32 v36, v42, v42
	v_add_f32_e32 v35, v35, v36
	v_add_f32_e32 v34, v34, v35
	v_add_f32_e32 v34, v38, v34
	s_nop 1
	v_add_f32_dpp v34, v34, v34 quad_perm:[1,0,3,2] row_mask:0xf bank_mask:0xf bound_ctrl:1
	s_nop 1
	v_add_f32_dpp v34, v34, v34 quad_perm:[2,3,0,1] row_mask:0xf bank_mask:0xf bound_ctrl:1
	s_nop 1
	v_add_f32_dpp v34, v34, v34 row_half_mirror row_mask:0xf bank_mask:0xf bound_ctrl:1
	s_nop 1
	v_add_f32_dpp v34, v34, v34 row_mirror row_mask:0xf bank_mask:0xf bound_ctrl:1
	s_nop 0
	v_readlane_b32 s16, v34, 0
	v_readlane_b32 s21, v34, 16
	v_readlane_b32 s20, v34, 32
	v_readlane_b32 s24, v34, 48
	s_and_saveexec_b64 s[22:23], s[26:27]
	s_cbranch_execz .LBB0_432
	v_mov_b32_e32 v35, s24
	v_mov_b32_e32 v34, s21
	v_add_f32_e32 v35, s20, v35
	v_readlane_b32 s20, v250, 17
	v_add_f32_e32 v34, s16, v34
	v_readlane_b32 s21, v250, 18
	s_nop 1
	v_cndmask_b32_e64 v34, v35, v34, s[20:21]
	v_fmamk_f32 v34, v34, 0x3a000000, v192
	v_mul_f32_e32 v35, 0x4f800000, v34
	v_rsq_f32_e32 v35, v34
	s_nop 0
	v_mul_f32_e32 v36, v34, v35
	v_fma_f32 v36, -v36, v35, 1.0
	v_mul_f32_e32 v37, 0.5, v35
	v_fma_f32 v34, v37, v36, v35
	v_subrev_u32_e32 v35, 64, v54
	ds_write_b32 v35, v34
; #define PM_UNPK(q_, f_) do { f_[0] = bflo(q_.x); f_[1] = bfhi(q_.x); f_[2] = bflo(q_.y); f_[3] = bfhi(q_.y); f_[4] = bflo(q_.z); f_[5] = bfhi(q_.z); f_[6] = bflo(q_.w); f_[7] = bfhi(q_.w); } while (0)
; template <bool XF32> ...
;     ...
;             for (int z = 0; z < 2; ++z) { float ss = 0.f;
; #pragma unroll
;                 for (int j = 0; j < (XF32 ? 16 : 8); ++j) { const v4u q = qq[z][j];
;                     if constexpr (XF32) { const f32x4 v = __builtin_bit_cast(f32x4, q); ss += (v.x * v.x + v.y * v.y) + (v.z * v.z + v.w * v.w); }
;                     else { float f[8]; PM_UNPK(q, f); ss += ((f[0] * f[0] + f[1] * f[1]) + (f[2] * f[2] + f[3] * f[3])) + ((f[4] * f[4] + f[5] * f[5]) + (f[6] * f[6] + f[7] * f[7])); } }
;                 ssq[z] = ss; }
; #pragma unroll
;             for (int z = 0; z < 2; ++z) { float ss = ssq[z];
;                 ss = half_sum(ss);
;                 const float rstd = 1.0f / sqrtf(ss * (1.0f / DM) + EPS);
;                 if (l31 == 0 && rrq[z] < 64 + halo) rstdL[rrq[z] + 15 - halo] = rstd; }
.LBB0_432:
	s_or_b64 exec, exec, s[22:23]
	s_waitcnt vmcnt(7)
	v_lshlrev_b32_e32 v34, 16, v30
	v_and_b32_e32 v30, 0xffff0000, v30
	v_lshlrev_b32_e32 v35, 16, v31
	v_and_b32_e32 v31, 0xffff0000, v31
	v_mul_f32_e32 v30, v30, v30
	v_mul_f32_e32 v31, v31, v31
	v_lshlrev_b32_e32 v36, 16, v32
	v_and_b32_e32 v32, 0xffff0000, v32
	v_lshlrev_b32_e32 v37, 16, v33
	v_and_b32_e32 v33, 0xffff0000, v33
	v_fmac_f32_e32 v30, v34, v34
	v_fmac_f32_e32 v31, v35, v35
	v_add_f32_e32 v30, v30, v31
	v_mul_f32_e32 v31, v32, v32
	v_mul_f32_e32 v32, v33, v33
	v_fmac_f32_e32 v31, v36, v36
	v_fmac_f32_e32 v32, v37, v37
	v_add_f32_e32 v31, v31, v32
	v_add_f32_e32 v30, v30, v31
	s_waitcnt vmcnt(6)
	v_lshlrev_b32_e32 v31, 16, v26
	v_and_b32_e32 v26, 0xffff0000, v26
	v_lshlrev_b32_e32 v32, 16, v27
	v_and_b32_e32 v27, 0xffff0000, v27
	v_mul_f32_e32 v26, v26, v26
	v_mul_f32_e32 v27, v27, v27
	v_lshlrev_b32_e32 v33, 16, v28
	v_and_b32_e32 v28, 0xffff0000, v28
	v_lshlrev_b32_e32 v34, 16, v29
	v_and_b32_e32 v29, 0xffff0000, v29
	v_fmac_f32_e32 v26, v31, v31
	v_fmac_f32_e32 v27, v32, v32
	v_add_f32_e32 v26, v26, v27
	v_mul_f32_e32 v27, v28, v28
	v_mul_f32_e32 v28, v29, v29
	v_fmac_f32_e32 v27, v33, v33
	v_fmac_f32_e32 v28, v34, v34
	v_add_f32_e32 v27, v27, v28
	v_add_f32_e32 v26, v26, v27
	s_waitcnt vmcnt(5)
	v_lshlrev_b32_e32 v27, 16, v22
	v_and_b32_e32 v22, 0xffff0000, v22
	v_lshlrev_b32_e32 v28, 16, v23
	v_and_b32_e32 v23, 0xffff0000, v23
	v_mul_f32_e32 v22, v22, v22
	v_mul_f32_e32 v23, v23, v23
	v_add_f32_e32 v26, v30, v26
	v_lshlrev_b32_e32 v29, 16, v24
	v_and_b32_e32 v24, 0xffff0000, v24
	v_lshlrev_b32_e32 v30, 16, v25
	v_and_b32_e32 v25, 0xffff0000, v25
	v_fmac_f32_e32 v22, v27, v27
	v_fmac_f32_e32 v23, v28, v28
	v_add_f32_e32 v22, v22, v23
	v_mul_f32_e32 v23, v24, v24
	v_mul_f32_e32 v24, v25, v25
	v_fmac_f32_e32 v23, v29, v29
	v_fmac_f32_e32 v24, v30, v30
	v_add_f32_e32 v23, v23, v24
	v_add_f32_e32 v22, v22, v23
	s_waitcnt vmcnt(4)
	v_lshlrev_b32_e32 v23, 16, v18
	v_and_b32_e32 v18, 0xffff0000, v18
	v_lshlrev_b32_e32 v24, 16, v19
	v_and_b32_e32 v19, 0xffff0000, v19
	v_mul_f32_e32 v18, v18, v18
	v_mul_f32_e32 v19, v19, v19
	v_add_f32_e32 v22, v26, v22
	v_lshlrev_b32_e32 v25, 16, v20
	v_and_b32_e32 v20, 0xffff0000, v20
	v_lshlrev_b32_e32 v26, 16, v21
	v_and_b32_e32 v21, 0xffff0000, v21
	v_fmac_f32_e32 v18, v23, v23
	v_fmac_f32_e32 v19, v24, v24
	v_add_f32_e32 v18, v18, v19
	v_mul_f32_e32 v19, v20, v20
	v_mul_f32_e32 v20, v21, v21
	v_fmac_f32_e32 v19, v25, v25
	v_fmac_f32_e32 v20, v26, v26
	v_add_f32_e32 v19, v19, v20
	v_add_f32_e32 v18, v18, v19
	s_waitcnt vmcnt(3)
	v_lshlrev_b32_e32 v19, 16, v14
	v_and_b32_e32 v14, 0xffff0000, v14
	v_lshlrev_b32_e32 v20, 16, v15
	v_and_b32_e32 v15, 0xffff0000, v15
	v_mul_f32_e32 v14, v14, v14
	v_mul_f32_e32 v15, v15, v15
	v_add_f32_e32 v18, v22, v18
	v_lshlrev_b32_e32 v21, 16, v16
	v_and_b32_e32 v16, 0xffff0000, v16
	v_lshlrev_b32_e32 v22, 16, v17
	v_and_b32_e32 v17, 0xffff0000, v17
	v_fmac_f32_e32 v14, v19, v19
	v_fmac_f32_e32 v15, v20, v20
	v_add_f32_e32 v14, v14, v15
	v_mul_f32_e32 v15, v16, v16
	v_mul_f32_e32 v16, v17, v17
	v_fmac_f32_e32 v15, v21, v21
	v_fmac_f32_e32 v16, v22, v22
	v_add_f32_e32 v15, v15, v16
	v_add_f32_e32 v14, v14, v15
	s_waitcnt vmcnt(2)
	v_lshlrev_b32_e32 v15, 16, v10
	v_and_b32_e32 v10, 0xffff0000, v10
	v_lshlrev_b32_e32 v16, 16, v11
	v_and_b32_e32 v11, 0xffff0000, v11
	v_mul_f32_e32 v10, v10, v10
	v_mul_f32_e32 v11, v11, v11
	v_add_f32_e32 v14, v18, v14
	v_lshlrev_b32_e32 v17, 16, v12
	v_and_b32_e32 v12, 0xffff0000, v12
	v_lshlrev_b32_e32 v18, 16, v13
	v_and_b32_e32 v13, 0xffff0000, v13
	v_fmac_f32_e32 v10, v15, v15
	v_fmac_f32_e32 v11, v16, v16
	v_add_f32_e32 v10, v10, v11
	v_mul_f32_e32 v11, v12, v12
	v_mul_f32_e32 v12, v13, v13
	v_fmac_f32_e32 v11, v17, v17
	v_fmac_f32_e32 v12, v18, v18
	v_add_f32_e32 v11, v11, v12
	v_add_f32_e32 v10, v10, v11
	s_waitcnt vmcnt(1)
	v_lshlrev_b32_e32 v11, 16, v6
	v_and_b32_e32 v6, 0xffff0000, v6
	v_lshlrev_b32_e32 v12, 16, v7
	v_and_b32_e32 v7, 0xffff0000, v7
	v_mul_f32_e32 v6, v6, v6
	v_mul_f32_e32 v7, v7, v7
	v_add_f32_e32 v10, v14, v10
	v_lshlrev_b32_e32 v13, 16, v8
	v_and_b32_e32 v8, 0xffff0000, v8
	v_lshlrev_b32_e32 v14, 16, v9
	v_and_b32_e32 v9, 0xffff0000, v9
	v_fmac_f32_e32 v6, v11, v11
	v_fmac_f32_e32 v7, v12, v12
	v_add_f32_e32 v6, v6, v7
	v_mul_f32_e32 v7, v8, v8
	v_mul_f32_e32 v8, v9, v9
	v_fmac_f32_e32 v7, v13, v13
	v_fmac_f32_e32 v8, v14, v14
	v_add_f32_e32 v7, v7, v8
	v_add_f32_e32 v6, v6, v7
	s_waitcnt vmcnt(0)
	v_lshlrev_b32_e32 v7, 16, v2
	v_and_b32_e32 v2, 0xffff0000, v2
	v_lshlrev_b32_e32 v8, 16, v3
	v_and_b32_e32 v3, 0xffff0000, v3
	v_mul_f32_e32 v2, v2, v2
	v_mul_f32_e32 v3, v3, v3
	v_add_f32_e32 v6, v10, v6
	v_lshlrev_b32_e32 v9, 16, v4
	v_and_b32_e32 v4, 0xffff0000, v4
	v_lshlrev_b32_e32 v10, 16, v5
	v_and_b32_e32 v5, 0xffff0000, v5
	v_fmac_f32_e32 v2, v7, v7
	v_fmac_f32_e32 v3, v8, v8
	v_add_f32_e32 v2, v2, v3
	v_mul_f32_e32 v3, v4, v4
	v_mul_f32_e32 v4, v5, v5
	v_fmac_f32_e32 v3, v9, v9
	v_fmac_f32_e32 v4, v10, v10
	v_add_f32_e32 v3, v3, v4
	v_add_f32_e32 v2, v2, v3
	v_add_f32_e32 v2, v6, v2
	s_nor_b64 s[26:27], s[36:37], s[44:45]
	s_nop 0
	v_add_f32_dpp v2, v2, v2 quad_perm:[1,0,3,2] row_mask:0xf bank_mask:0xf bound_ctrl:1
	s_nop 1
	v_add_f32_dpp v2, v2, v2 quad_perm:[2,3,0,1] row_mask:0xf bank_mask:0xf bound_ctrl:1
	s_nop 1
	v_add_f32_dpp v2, v2, v2 row_half_mirror row_mask:0xf bank_mask:0xf bound_ctrl:1
	s_nop 1
	v_add_f32_dpp v2, v2, v2 row_mirror row_mask:0xf bank_mask:0xf bound_ctrl:1
	s_nop 0
	v_readlane_b32 s16, v2, 0
	v_readlane_b32 s21, v2, 16
	v_readlane_b32 s20, v2, 32
	v_readlane_b32 s24, v2, 48
	s_and_saveexec_b64 s[22:23], s[26:27]
	s_cbranch_execz .LBB0_429
	v_mov_b32_e32 v3, s24
	v_mov_b32_e32 v2, s21
	v_add_f32_e32 v3, s20, v3
	v_readlane_b32 s20, v250, 17
	v_add_f32_e32 v2, s16, v2
	v_readlane_b32 s21, v250, 18
	s_nop 1
	v_cndmask_b32_e64 v2, v3, v2, s[20:21]
	v_fmamk_f32 v2, v2, 0x3a000000, v192
	v_mul_f32_e32 v3, 0x4f800000, v2
	v_rsq_f32_e32 v3, v2
	s_nop 0
	v_mul_f32_e32 v4, v2, v3
	v_fma_f32 v4, -v4, v3, 1.0
	v_mul_f32_e32 v5, 0.5, v3
	v_fma_f32 v2, v5, v4, v3
	ds_write_b32 v54, v2
	s_branch .LBB0_429

; #define GAS __attribute__((address_space(1)))
; __device__ __forceinline__ unsigned pk2(float lo, float hi) { const pk_f2 v = {lo, hi}; return __builtin_bit_cast(unsigned, __builtin_convertvector(v, pk_b2)); }
; __device__ __forceinline__ float silu1(float x) { return x * sigmoid_f(x); }
; __device__ __forceinline__ float wave_sum(float v) { v = row16_sum(v); return (WS_RL(v, 0) + WS_RL(v, 16)) + (WS_RL(v, 32) + WS_RL(v, 48)); }
; __device__ __forceinline__ void phase_ret_post(const bf16* O, const bf16* PROJ, const float* ng, bf16* Pb, int gw, int NGW, int lane) {
;     ...
;     for (int m = gw; m < M; m += NGW) {
;         const GAS v4u* orow = (const GAS v4u*)(O + (size_t)m * RT_V) + lane;
;         const GAS v4u* grow = (const GAS v4u*)(PROJ + (size_t)m * RT_IN + 8192) + lane;
;         GAS v4u* prow = (GAS v4u*)(Pb + (size_t)m * RT_V) + lane;
;         v4u ob[8], gq[8];
; #pragma unroll
;         for (int hh = 0; hh < 8; ++hh) { ob[hh] = orow[64 * hh]; gq[hh] = grow[64 * hh]; }
; #pragma unroll
;         for (int hh = 0; hh < 8; ++hh) {
;             const f32x4 o0 = (f32x4){bflo(ob[hh].x), bfhi(ob[hh].x), bflo(ob[hh].y), bfhi(ob[hh].y)}, o1 = (f32x4){bflo(ob[hh].z), bfhi(ob[hh].z), bflo(ob[hh].w), bfhi(ob[hh].w)};
;             const float ss = ((o0.x * o0.x + o0.y * o0.y) + (o0.z * o0.z + o0.w * o0.w)) + ((o1.x * o1.x + o1.y * o1.y) + (o1.z * o1.z + o1.w * o1.w));
;             const float rstd = 1.0f / sqrtf(wave_sum(ss) * (1.0f / 512.0f) + EPS);
;             const v4u g = gq[hh];
;             v4u w; w.x = pk2(o0.x * rstd * nv[hh][0].x * silu1(bflo(g.x)), o0.y * rstd * nv[hh][0].y * silu1(bfhi(g.x))); w.y = pk2(o0.z * rstd * nv[hh][0].z * silu1(bflo(g.y)), o0.w * rstd * nv[hh][0].w * silu1(bfhi(g.y)));
;             w.z = pk2(o1.x * rstd * nv[hh][1].x * silu1(bflo(g.z)), o1.y * rstd * nv[hh][1].y * silu1(bfhi(g.z))); w.w = pk2(o1.z * rstd * nv[hh][1].z * silu1(bflo(g.w)), o1.w * rstd * nv[hh][1].w * silu1(bfhi(g.w)));
;             prow[64 * hh] = w;
.LBB0_856:
	v_lshl_add_u64 v[130:131], s[44:45], 0, v[128:129]
	v_add_co_u32_e32 v68, vcc, 0x3c800000, v130
	v_lshl_add_u64 v[66:67], s[18:19], 0, v[128:129]
	s_nop 0
	v_addc_co_u32_e32 v69, vcc, 0, v131, vcc
	global_load_dwordx4 v[122:125], v[68:69], off
	v_add_co_u32_e32 v70, vcc, 0x24804000, v66
	s_mov_b32 s1, 0x3c801000
	s_nop 0
	v_addc_co_u32_e32 v71, vcc, 0, v67, vcc
	global_load_dwordx4 v[132:135], v[70:71], off
	global_load_dwordx4 v[118:121], v[68:69], off offset:1024
	global_load_dwordx4 v[114:117], v[70:71], off offset:1024
	global_load_dwordx4 v[110:113], v[68:69], off offset:2048
	global_load_dwordx4 v[106:109], v[70:71], off offset:2048
	global_load_dwordx4 v[102:105], v[68:69], off offset:3072
	global_load_dwordx4 v[98:101], v[70:71], off offset:3072
	v_add_co_u32_e32 v68, vcc, s1, v130
	s_mov_b32 s1, 0x24805000
	s_nop 0
	v_addc_co_u32_e32 v69, vcc, 0, v131, vcc
	v_add_co_u32_e32 v66, vcc, s1, v66
	global_load_dwordx4 v[94:97], v[68:69], off
	s_nop 0
	v_addc_co_u32_e32 v67, vcc, 0, v67, vcc
	global_load_dwordx4 v[90:93], v[66:67], off
	global_load_dwordx4 v[86:89], v[68:69], off offset:1024
	global_load_dwordx4 v[82:85], v[66:67], off offset:1024
	global_load_dwordx4 v[78:81], v[68:69], off offset:2048
	global_load_dwordx4 v[74:77], v[66:67], off offset:2048
	global_load_dwordx4 v[70:73], v[68:69], off offset:3072
	s_nop 0
	global_load_dwordx4 v[66:69], v[66:67], off offset:3072
	s_add_i32 s0, s0, s58
	s_waitcnt vmcnt(14)
	v_lshlrev_b32_e32 v142, 16, v133
	v_lshlrev_b32_e32 v138, 16, v124
	v_and_b32_e32 v139, 0xffff0000, v124
	v_lshlrev_b32_e32 v124, 16, v134
	v_mul_f32_e32 v0, 0xbfb8aa3b, v124
	v_exp_f32_e32 v0, v0
	v_lshlrev_b32_e32 v136, 16, v125
	v_and_b32_e32 v137, 0xffff0000, v125
	v_and_b32_e32 v125, 0xffff0000, v134
	v_add_f32_e32 v0, 1.0, v0
	v_rcp_f32_e32 v140, v0
	v_mul_f32_e32 v0, 0xbfb8aa3b, v125
	v_exp_f32_e32 v0, v0
	v_and_b32_e32 v143, 0xffff0000, v133
	v_mov_b32_e32 v147, v137
	v_mov_b32_e32 v149, v139
	v_add_f32_e32 v0, 1.0, v0
	v_rcp_f32_e32 v141, v0
	v_mul_f32_e32 v0, 0xbfb8aa3b, v142
	v_exp_f32_e32 v0, v0
	v_pk_mul_f32 v[124:125], v[140:141], v[124:125]
	v_lshlrev_b32_e32 v140, 16, v123
	v_add_f32_e32 v0, 1.0, v0
	v_rcp_f32_e32 v144, v0
	v_mul_f32_e32 v0, 0xbfb8aa3b, v143
	v_exp_f32_e32 v0, v0
	v_and_b32_e32 v141, 0xffff0000, v123
	v_and_b32_e32 v123, 0xffff0000, v132
	v_mov_b32_e32 v146, v141
	v_add_f32_e32 v0, 1.0, v0
	v_rcp_f32_e32 v145, v0
	v_pk_mul_f32 v[146:147], v[146:147], v[146:147]
	v_pk_mul_f32 v[142:143], v[144:145], v[142:143]
	v_lshlrev_b32_e32 v144, 16, v122
	v_and_b32_e32 v145, 0xffff0000, v122
	v_lshlrev_b32_e32 v122, 16, v132
	v_mul_f32_e32 v0, 0xbfb8aa3b, v122
	v_exp_f32_e32 v0, v0
	v_mov_b32_e32 v148, v145
	v_pk_mul_f32 v[148:149], v[148:149], v[148:149]
	v_add_f32_e32 v0, 1.0, v0
	v_rcp_f32_e32 v132, v0
	v_mul_f32_e32 v0, 0xbfb8aa3b, v123
	v_exp_f32_e32 v0, v0
	s_nop 0
	v_add_f32_e32 v0, 1.0, v0
	v_rcp_f32_e32 v133, v0
	s_nop 0
	v_pk_mul_f32 v[122:123], v[132:133], v[122:123]
	v_mov_b32_e32 v132, v140
	v_mov_b32_e32 v133, v136
	v_pk_fma_f32 v[132:133], v[132:133], v[132:133], v[146:147]
	v_mov_b32_e32 v146, v144
	v_mov_b32_e32 v147, v138
	v_pk_fma_f32 v[146:147], v[146:147], v[146:147], v[148:149]
	s_nop 0
	v_pk_add_f32 v[132:133], v[146:147], v[132:133]
	s_nop 0
	v_add_f32_e32 v0, v132, v133
	s_nop 1
	v_add_f32_dpp v0, v0, v0 quad_perm:[1,0,3,2] row_mask:0xf bank_mask:0xf bound_ctrl:1
	s_nop 1
	v_add_f32_dpp v0, v0, v0 quad_perm:[2,3,0,1] row_mask:0xf bank_mask:0xf bound_ctrl:1
	s_nop 1
	v_add_f32_dpp v0, v0, v0 row_half_mirror row_mask:0xf bank_mask:0xf bound_ctrl:1
	s_nop 1
	v_add_f32_dpp v0, v0, v0 row_mirror row_mask:0xf bank_mask:0xf bound_ctrl:1
	s_nop 0
	v_readlane_b32 s1, v0, 16
	v_readlane_b32 s4, v0, 48
	v_readlane_b32 s2, v0, 0
	v_readlane_b32 s3, v0, 32
	v_mov_b32_e32 v132, s1
	v_mov_b32_e32 v133, s4
	v_pk_add_f32 v[132:133], s[2:3], v[132:133]
	s_mov_b32 s1, 0x1c801000
	v_add_f32_e32 v0, v132, v133
	v_fmamk_f32 v0, v0, 0x3b000000, v192
	v_rsq_f32_e32 v127, v0
	s_nop 0
	v_mul_f32_e32 v132, v0, v127
	v_fma_f32 v132, -v132, v127, 1.0
	v_mul_f32_e32 v133, 0.5, v127
	v_fma_f32 v0, v133, v132, v127
	v_pk_mul_f32 v[132:133], v[0:1], v[144:145] op_sel_hi:[0,1]
	v_pk_mul_f32 v[132:133], v[58:59], v[132:133]
	v_pk_mul_f32 v[136:137], v[0:1], v[136:137] op_sel_hi:[0,1]
	v_pk_mul_f32 v[122:123], v[122:123], v[132:133]
	v_pk_mul_f32 v[132:133], v[0:1], v[140:141] op_sel_hi:[0,1]
	v_pk_mul_f32 v[132:133], v[60:61], v[132:133]
	v_cvt_pk_bf16_f32 v122, v122, v123
	v_pk_mul_f32 v[132:133], v[142:143], v[132:133]
	v_pk_mul_f32 v[136:137], v[64:65], v[136:137]
	v_cvt_pk_bf16_f32 v123, v132, v133
	v_pk_mul_f32 v[132:133], v[0:1], v[138:139] op_sel_hi:[0,1]
	v_pk_mul_f32 v[132:133], v[62:63], v[132:133]
	s_nop 0
	v_pk_mul_f32 v[124:125], v[124:125], v[132:133]
	v_lshlrev_b32_e32 v132, 16, v135
	v_and_b32_e32 v133, 0xffff0000, v135
	v_cvt_pk_bf16_f32 v124, v124, v125
	v_mul_f32_e32 v125, 0xbfb8aa3b, v132
	v_mul_f32_e32 v0, 0xbfb8aa3b, v133
	v_exp_f32_e32 v125, v125
	v_exp_f32_e32 v0, v0
	v_add_f32_e32 v125, 1.0, v125
	v_add_f32_e32 v0, 1.0, v0
	v_rcp_f32_e32 v134, v125
	v_rcp_f32_e32 v135, v0
	s_nop 0
	v_pk_mul_f32 v[132:133], v[134:135], v[132:133]
	s_nop 0
	v_pk_mul_f32 v[132:133], v[132:133], v[136:137]
	s_waitcnt vmcnt(12)
; __device__ __forceinline__ unsigned pk2(float lo, float hi) { const pk_f2 v = {lo, hi}; return __builtin_bit_cast(unsigned, __builtin_convertvector(v, pk_b2)); }
; __device__ __forceinline__ float silu1(float x) { return x * sigmoid_f(x); }
; __device__ __forceinline__ float wave_sum(float v) { v = row16_sum(v); return (WS_RL(v, 0) + WS_RL(v, 16)) + (WS_RL(v, 32) + WS_RL(v, 48)); }
; __device__ __forceinline__ void phase_ret_post(const bf16* O, const bf16* PROJ, const float* ng, bf16* Pb, int gw, int NGW, int lane) {
;     ...
;         for (int hh = 0; hh < 8; ++hh) {
;             const f32x4 o0 = (f32x4){bflo(ob[hh].x), bfhi(ob[hh].x), bflo(ob[hh].y), bfhi(ob[hh].y)}, o1 = (f32x4){bflo(ob[hh].z), bfhi(ob[hh].z), bflo(ob[hh].w), bfhi(ob[hh].w)};
;             const float ss = ((o0.x * o0.x + o0.y * o0.y) + (o0.z * o0.z + o0.w * o0.w)) + ((o1.x * o1.x + o1.y * o1.y) + (o1.z * o1.z + o1.w * o1.w));
;             const float rstd = 1.0f / sqrtf(wave_sum(ss) * (1.0f / 512.0f) + EPS);
;             const v4u g = gq[hh];
;             v4u w; w.x = pk2(o0.x * rstd * nv[hh][0].x * silu1(bflo(g.x)), o0.y * rstd * nv[hh][0].y * silu1(bfhi(g.x))); w.y = pk2(o0.z * rstd * nv[hh][0].z * silu1(bflo(g.y)), o0.w * rstd * nv[hh][0].w * silu1(bfhi(g.y)));
;             w.z = pk2(o1.x * rstd * nv[hh][1].x * silu1(bflo(g.z)), o1.y * rstd * nv[hh][1].y * silu1(bfhi(g.z))); w.w = pk2(o1.z * rstd * nv[hh][1].z * silu1(bflo(g.w)), o1.w * rstd * nv[hh][1].w * silu1(bfhi(g.w)));
;             prow[64 * hh] = w;
	v_lshlrev_b32_e32 v136, 16, v115
	v_cvt_pk_bf16_f32 v125, v132, v133
	v_add_co_u32_e32 v132, vcc, s7, v130
	v_and_b32_e32 v137, 0xffff0000, v115
	s_nop 0
	v_addc_co_u32_e32 v133, vcc, 0, v131, vcc
	v_add_co_u32_e32 v130, vcc, s1, v130
	s_nop 1
	v_addc_co_u32_e32 v131, vcc, 0, v131, vcc
	global_store_dwordx4 v[130:131], v[122:125], off offset:-4096
	s_nop 1
	v_lshlrev_b32_e32 v124, 16, v120
	v_and_b32_e32 v125, 0xffff0000, v120
	v_lshlrev_b32_e32 v120, 16, v116
	v_mul_f32_e32 v0, 0xbfb8aa3b, v120
	v_exp_f32_e32 v0, v0
	v_lshlrev_b32_e32 v122, 16, v121
	v_and_b32_e32 v123, 0xffff0000, v121
	v_and_b32_e32 v121, 0xffff0000, v116
	v_add_f32_e32 v0, 1.0, v0
	v_rcp_f32_e32 v134, v0
	v_mul_f32_e32 v0, 0xbfb8aa3b, v121
	v_exp_f32_e32 v0, v0
	v_mov_b32_e32 v141, v123
	v_mov_b32_e32 v143, v125
	v_add_f32_e32 v0, 1.0, v0
	v_rcp_f32_e32 v135, v0
	v_mul_f32_e32 v0, 0xbfb8aa3b, v136
	v_exp_f32_e32 v0, v0
	v_pk_mul_f32 v[120:121], v[134:135], v[120:121]
	v_lshlrev_b32_e32 v134, 16, v119
	v_add_f32_e32 v0, 1.0, v0
	v_rcp_f32_e32 v138, v0
	v_mul_f32_e32 v0, 0xbfb8aa3b, v137
	v_exp_f32_e32 v0, v0
	v_and_b32_e32 v135, 0xffff0000, v119
	v_and_b32_e32 v119, 0xffff0000, v114
	v_mov_b32_e32 v140, v135
	v_add_f32_e32 v0, 1.0, v0
	v_rcp_f32_e32 v139, v0
	v_pk_mul_f32 v[140:141], v[140:141], v[140:141]
	v_pk_mul_f32 v[136:137], v[138:139], v[136:137]
	v_lshlrev_b32_e32 v138, 16, v118
	v_and_b32_e32 v139, 0xffff0000, v118
	v_lshlrev_b32_e32 v118, 16, v114
	v_mul_f32_e32 v0, 0xbfb8aa3b, v118
	v_exp_f32_e32 v0, v0
	v_mov_b32_e32 v142, v139
	v_pk_mul_f32 v[142:143], v[142:143], v[142:143]
	v_add_f32_e32 v0, 1.0, v0
	v_rcp_f32_e32 v114, v0
	v_mul_f32_e32 v0, 0xbfb8aa3b, v119
	v_exp_f32_e32 v0, v0
	s_nop 0
	v_add_f32_e32 v0, 1.0, v0
	v_rcp_f32_e32 v115, v0
	s_nop 0
	v_pk_mul_f32 v[114:115], v[114:115], v[118:119]
	v_mov_b32_e32 v118, v134
	v_mov_b32_e32 v119, v122
	v_pk_fma_f32 v[118:119], v[118:119], v[118:119], v[140:141]
	v_mov_b32_e32 v140, v138
	v_mov_b32_e32 v141, v124
	v_pk_fma_f32 v[140:141], v[140:141], v[140:141], v[142:143]
	s_nop 0
	v_pk_add_f32 v[118:119], v[140:141], v[118:119]
	s_nop 0
	v_add_f32_e32 v0, v118, v119
	s_nop 1
	v_add_f32_dpp v0, v0, v0 quad_perm:[1,0,3,2] row_mask:0xf bank_mask:0xf bound_ctrl:1
	s_nop 1
	v_add_f32_dpp v0, v0, v0 quad_perm:[2,3,0,1] row_mask:0xf bank_mask:0xf bound_ctrl:1
	s_nop 1
	v_add_f32_dpp v0, v0, v0 row_half_mirror row_mask:0xf bank_mask:0xf bound_ctrl:1
	s_nop 1
	v_add_f32_dpp v0, v0, v0 row_mirror row_mask:0xf bank_mask:0xf bound_ctrl:1
	s_nop 0
	v_readlane_b32 s1, v0, 16
	v_readlane_b32 s4, v0, 48
	v_readlane_b32 s2, v0, 0
	v_readlane_b32 s3, v0, 32
	v_mov_b32_e32 v118, s1
	v_mov_b32_e32 v119, s4
	v_pk_add_f32 v[118:119], s[2:3], v[118:119]
	s_nop 0
	v_add_f32_e32 v0, v118, v119
	v_fmamk_f32 v0, v0, 0x3b000000, v192
	v_rsq_f32_e32 v116, v0
	s_nop 0
	v_mul_f32_e32 v118, v0, v116
	v_fma_f32 v118, -v118, v116, 1.0
	v_mul_f32_e32 v119, 0.5, v116
	v_fma_f32 v0, v119, v118, v116
	v_pk_mul_f32 v[118:119], v[0:1], v[138:139] op_sel_hi:[0,1]
	v_pk_mul_f32 v[118:119], v[50:51], v[118:119]
	v_pk_mul_f32 v[122:123], v[0:1], v[122:123] op_sel_hi:[0,1]
	v_pk_mul_f32 v[114:115], v[114:115], v[118:119]
	v_pk_mul_f32 v[118:119], v[0:1], v[134:135] op_sel_hi:[0,1]
	v_pk_mul_f32 v[118:119], v[52:53], v[118:119]
	v_cvt_pk_bf16_f32 v114, v114, v115
	v_pk_mul_f32 v[118:119], v[136:137], v[118:119]
	v_pk_mul_f32 v[122:123], v[56:57], v[122:123]
	v_cvt_pk_bf16_f32 v115, v118, v119
	v_pk_mul_f32 v[118:119], v[0:1], v[124:125] op_sel_hi:[0,1]
	v_pk_mul_f32 v[118:119], v[54:55], v[118:119]
	s_nop 0
	v_pk_mul_f32 v[118:119], v[120:121], v[118:119]
	s_nop 0
	v_cvt_pk_bf16_f32 v116, v118, v119
	v_lshlrev_b32_e32 v118, 16, v117
	v_and_b32_e32 v119, 0xffff0000, v117
	v_mul_f32_e32 v117, 0xbfb8aa3b, v118
	v_mul_f32_e32 v0, 0xbfb8aa3b, v119
	v_exp_f32_e32 v117, v117
	v_exp_f32_e32 v0, v0
	v_add_f32_e32 v117, 1.0, v117
	v_add_f32_e32 v0, 1.0, v0
	v_rcp_f32_e32 v120, v117
	v_rcp_f32_e32 v121, v0
	s_nop 0
	v_pk_mul_f32 v[118:119], v[120:121], v[118:119]
	s_nop 0
	v_pk_mul_f32 v[118:119], v[118:119], v[122:123]
	s_waitcnt vmcnt(11)
	v_lshlrev_b32_e32 v120, 16, v107
	v_cvt_pk_bf16_f32 v117, v118, v119
	global_store_dwordx4 v[132:133], v[114:117], off offset:1024
	v_and_b32_e32 v121, 0xffff0000, v107
	s_nop 0
	v_lshlrev_b32_e32 v116, 16, v112
	v_and_b32_e32 v117, 0xffff0000, v112
	v_lshlrev_b32_e32 v112, 16, v108
	v_mul_f32_e32 v0, 0xbfb8aa3b, v112
	v_exp_f32_e32 v0, v0
	v_lshlrev_b32_e32 v114, 16, v113
	v_and_b32_e32 v115, 0xffff0000, v113
	v_and_b32_e32 v113, 0xffff0000, v108
	v_add_f32_e32 v0, 1.0, v0
	v_rcp_f32_e32 v118, v0
	v_mul_f32_e32 v0, 0xbfb8aa3b, v113
	v_exp_f32_e32 v0, v0
	v_mov_b32_e32 v125, v115
	v_mov_b32_e32 v135, v117
	v_add_f32_e32 v0, 1.0, v0
	v_rcp_f32_e32 v119, v0
	v_mul_f32_e32 v0, 0xbfb8aa3b, v120
	v_exp_f32_e32 v0, v0
	v_pk_mul_f32 v[112:113], v[118:119], v[112:113]
	v_lshlrev_b32_e32 v118, 16, v111
	v_add_f32_e32 v0, 1.0, v0
	v_rcp_f32_e32 v122, v0
	v_mul_f32_e32 v0, 0xbfb8aa3b, v121
	v_exp_f32_e32 v0, v0
	v_and_b32_e32 v119, 0xffff0000, v111
	v_and_b32_e32 v111, 0xffff0000, v106
	v_mov_b32_e32 v124, v119
	v_add_f32_e32 v0, 1.0, v0
	v_rcp_f32_e32 v123, v0
	v_pk_mul_f32 v[124:125], v[124:125], v[124:125]
	v_pk_mul_f32 v[120:121], v[122:123], v[120:121]
	v_lshlrev_b32_e32 v122, 16, v110
	v_and_b32_e32 v123, 0xffff0000, v110
	v_lshlrev_b32_e32 v110, 16, v106
	v_mul_f32_e32 v0, 0xbfb8aa3b, v110
	v_exp_f32_e32 v0, v0
	v_mov_b32_e32 v134, v123
	v_pk_mul_f32 v[134:135], v[134:135], v[134:135]
	v_add_f32_e32 v0, 1.0, v0
	v_rcp_f32_e32 v106, v0
	v_mul_f32_e32 v0, 0xbfb8aa3b, v111
	v_exp_f32_e32 v0, v0
	s_nop 0
	v_add_f32_e32 v0, 1.0, v0
; __device__ __forceinline__ unsigned pk2(float lo, float hi) { const pk_f2 v = {lo, hi}; return __builtin_bit_cast(unsigned, __builtin_convertvector(v, pk_b2)); }
; __device__ __forceinline__ float silu1(float x) { return x * sigmoid_f(x); }
; __device__ __forceinline__ float wave_sum(float v) { v = row16_sum(v); return (WS_RL(v, 0) + WS_RL(v, 16)) + (WS_RL(v, 32) + WS_RL(v, 48)); }
; __device__ __forceinline__ void phase_ret_post(const bf16* O, const bf16* PROJ, const float* ng, bf16* Pb, int gw, int NGW, int lane) {
;     ...
;         for (int hh = 0; hh < 8; ++hh) {
;             const f32x4 o0 = (f32x4){bflo(ob[hh].x), bfhi(ob[hh].x), bflo(ob[hh].y), bfhi(ob[hh].y)}, o1 = (f32x4){bflo(ob[hh].z), bfhi(ob[hh].z), bflo(ob[hh].w), bfhi(ob[hh].w)};
;             const float ss = ((o0.x * o0.x + o0.y * o0.y) + (o0.z * o0.z + o0.w * o0.w)) + ((o1.x * o1.x + o1.y * o1.y) + (o1.z * o1.z + o1.w * o1.w));
;             const float rstd = 1.0f / sqrtf(wave_sum(ss) * (1.0f / 512.0f) + EPS);
;             const v4u g = gq[hh];
;             v4u w; w.x = pk2(o0.x * rstd * nv[hh][0].x * silu1(bflo(g.x)), o0.y * rstd * nv[hh][0].y * silu1(bfhi(g.x))); w.y = pk2(o0.z * rstd * nv[hh][0].z * silu1(bflo(g.y)), o0.w * rstd * nv[hh][0].w * silu1(bfhi(g.y)));
;             w.z = pk2(o1.x * rstd * nv[hh][1].x * silu1(bflo(g.z)), o1.y * rstd * nv[hh][1].y * silu1(bfhi(g.z))); w.w = pk2(o1.z * rstd * nv[hh][1].z * silu1(bflo(g.w)), o1.w * rstd * nv[hh][1].w * silu1(bfhi(g.w)));
;             prow[64 * hh] = w;
	v_rcp_f32_e32 v107, v0
	s_nop 0
	v_pk_mul_f32 v[106:107], v[106:107], v[110:111]
	v_mov_b32_e32 v110, v118
	v_mov_b32_e32 v111, v114
	v_pk_fma_f32 v[110:111], v[110:111], v[110:111], v[124:125]
	v_mov_b32_e32 v124, v122
	v_mov_b32_e32 v125, v116
	v_pk_fma_f32 v[124:125], v[124:125], v[124:125], v[134:135]
	s_nop 0
	v_pk_add_f32 v[110:111], v[124:125], v[110:111]
	s_nop 0
	v_add_f32_e32 v0, v110, v111
	s_nop 1
	v_add_f32_dpp v0, v0, v0 quad_perm:[1,0,3,2] row_mask:0xf bank_mask:0xf bound_ctrl:1
	s_nop 1
	v_add_f32_dpp v0, v0, v0 quad_perm:[2,3,0,1] row_mask:0xf bank_mask:0xf bound_ctrl:1
	s_nop 1
	v_add_f32_dpp v0, v0, v0 row_half_mirror row_mask:0xf bank_mask:0xf bound_ctrl:1
	s_nop 1
	v_add_f32_dpp v0, v0, v0 row_mirror row_mask:0xf bank_mask:0xf bound_ctrl:1
	s_nop 0
	v_readlane_b32 s1, v0, 16
	v_readlane_b32 s4, v0, 48
	v_readlane_b32 s2, v0, 0
	v_readlane_b32 s3, v0, 32
	v_mov_b32_e32 v110, s1
	v_mov_b32_e32 v111, s4
	v_pk_add_f32 v[110:111], s[2:3], v[110:111]
	s_nop 0
	v_add_f32_e32 v0, v110, v111
	v_fmamk_f32 v0, v0, 0x3b000000, v192
	v_rsq_f32_e32 v108, v0
	s_nop 0
	v_mul_f32_e32 v110, v0, v108
	v_fma_f32 v110, -v110, v108, 1.0
	v_mul_f32_e32 v111, 0.5, v108
	v_fma_f32 v0, v111, v110, v108
	v_pk_mul_f32 v[110:111], v[0:1], v[122:123] op_sel_hi:[0,1]
	v_pk_mul_f32 v[110:111], v[38:39], v[110:111]
	v_pk_mul_f32 v[114:115], v[0:1], v[114:115] op_sel_hi:[0,1]
	v_pk_mul_f32 v[106:107], v[106:107], v[110:111]
	v_pk_mul_f32 v[110:111], v[0:1], v[118:119] op_sel_hi:[0,1]
	v_pk_mul_f32 v[110:111], v[40:41], v[110:111]
	v_cvt_pk_bf16_f32 v106, v106, v107
	v_pk_mul_f32 v[110:111], v[120:121], v[110:111]
	v_pk_mul_f32 v[114:115], v[48:49], v[114:115]
	v_cvt_pk_bf16_f32 v107, v110, v111
	v_pk_mul_f32 v[110:111], v[0:1], v[116:117] op_sel_hi:[0,1]
	v_pk_mul_f32 v[110:111], v[46:47], v[110:111]
	s_nop 0
	v_pk_mul_f32 v[110:111], v[112:113], v[110:111]
	s_nop 0
	v_cvt_pk_bf16_f32 v108, v110, v111
	v_lshlrev_b32_e32 v110, 16, v109
	v_and_b32_e32 v111, 0xffff0000, v109
	v_mul_f32_e32 v109, 0xbfb8aa3b, v110
	v_mul_f32_e32 v0, 0xbfb8aa3b, v111
	v_exp_f32_e32 v109, v109
	v_exp_f32_e32 v0, v0
	v_add_f32_e32 v109, 1.0, v109
	v_add_f32_e32 v0, 1.0, v0
	v_rcp_f32_e32 v112, v109
	v_rcp_f32_e32 v113, v0
	s_nop 0
	v_pk_mul_f32 v[110:111], v[112:113], v[110:111]
	s_nop 0
	v_pk_mul_f32 v[110:111], v[110:111], v[114:115]
	s_waitcnt vmcnt(10)
	v_lshlrev_b32_e32 v112, 16, v99
	v_cvt_pk_bf16_f32 v109, v110, v111
	global_store_dwordx4 v[132:133], v[106:109], off offset:2048
	v_and_b32_e32 v113, 0xffff0000, v99
	s_nop 0
	v_lshlrev_b32_e32 v108, 16, v104
	v_and_b32_e32 v109, 0xffff0000, v104
	v_lshlrev_b32_e32 v104, 16, v100
	v_mul_f32_e32 v0, 0xbfb8aa3b, v104
	v_exp_f32_e32 v0, v0
	v_lshlrev_b32_e32 v106, 16, v105
	v_and_b32_e32 v107, 0xffff0000, v105
	v_and_b32_e32 v105, 0xffff0000, v100
	v_add_f32_e32 v0, 1.0, v0
	v_rcp_f32_e32 v110, v0
	v_mul_f32_e32 v0, 0xbfb8aa3b, v105
	v_exp_f32_e32 v0, v0
	v_mov_b32_e32 v117, v107
	v_mov_b32_e32 v119, v109
	v_add_f32_e32 v0, 1.0, v0
	v_rcp_f32_e32 v111, v0
	v_mul_f32_e32 v0, 0xbfb8aa3b, v112
	v_exp_f32_e32 v0, v0
	v_pk_mul_f32 v[104:105], v[110:111], v[104:105]
	v_lshlrev_b32_e32 v110, 16, v103
	v_add_f32_e32 v0, 1.0, v0
	v_rcp_f32_e32 v114, v0
	v_mul_f32_e32 v0, 0xbfb8aa3b, v113
	v_exp_f32_e32 v0, v0
	v_and_b32_e32 v111, 0xffff0000, v103
	v_and_b32_e32 v103, 0xffff0000, v98
	v_mov_b32_e32 v116, v111
	v_add_f32_e32 v0, 1.0, v0
	v_rcp_f32_e32 v115, v0
	v_pk_mul_f32 v[116:117], v[116:117], v[116:117]
	v_pk_mul_f32 v[112:113], v[114:115], v[112:113]
	v_lshlrev_b32_e32 v114, 16, v102
	v_and_b32_e32 v115, 0xffff0000, v102
	v_lshlrev_b32_e32 v102, 16, v98
	v_mul_f32_e32 v0, 0xbfb8aa3b, v102
	v_exp_f32_e32 v0, v0
	v_mov_b32_e32 v118, v115
	v_pk_mul_f32 v[118:119], v[118:119], v[118:119]
	v_add_f32_e32 v0, 1.0, v0
	v_rcp_f32_e32 v98, v0
	v_mul_f32_e32 v0, 0xbfb8aa3b, v103
	v_exp_f32_e32 v0, v0
	s_nop 0
	v_add_f32_e32 v0, 1.0, v0
	v_rcp_f32_e32 v99, v0
	s_nop 0
	v_pk_mul_f32 v[98:99], v[98:99], v[102:103]
	v_mov_b32_e32 v102, v110
	v_mov_b32_e32 v103, v106
	v_pk_fma_f32 v[102:103], v[102:103], v[102:103], v[116:117]
	v_mov_b32_e32 v116, v114
	v_mov_b32_e32 v117, v108
	v_pk_fma_f32 v[116:117], v[116:117], v[116:117], v[118:119]
	s_nop 0
	v_pk_add_f32 v[102:103], v[116:117], v[102:103]
	s_nop 0
	v_add_f32_e32 v0, v102, v103
	s_nop 1
	v_add_f32_dpp v0, v0, v0 quad_perm:[1,0,3,2] row_mask:0xf bank_mask:0xf bound_ctrl:1
	s_nop 1
	v_add_f32_dpp v0, v0, v0 quad_perm:[2,3,0,1] row_mask:0xf bank_mask:0xf bound_ctrl:1
	s_nop 1
	v_add_f32_dpp v0, v0, v0 row_half_mirror row_mask:0xf bank_mask:0xf bound_ctrl:1
	s_nop 1
	v_add_f32_dpp v0, v0, v0 row_mirror row_mask:0xf bank_mask:0xf bound_ctrl:1
	s_nop 0
	v_readlane_b32 s1, v0, 16
	v_readlane_b32 s4, v0, 48
	v_readlane_b32 s2, v0, 0
	v_readlane_b32 s3, v0, 32
	v_mov_b32_e32 v102, s1
	v_mov_b32_e32 v103, s4
	v_pk_add_f32 v[102:103], s[2:3], v[102:103]
	s_nop 0
	v_add_f32_e32 v0, v102, v103
	v_fmamk_f32 v0, v0, 0x3b000000, v192
	v_rsq_f32_e32 v100, v0
	s_nop 0
	v_mul_f32_e32 v102, v0, v100
	v_fma_f32 v102, -v102, v100, 1.0
	v_mul_f32_e32 v103, 0.5, v100
	v_fma_f32 v0, v103, v102, v100
	v_pk_mul_f32 v[102:103], v[0:1], v[114:115] op_sel_hi:[0,1]
	v_pk_mul_f32 v[102:103], v[42:43], v[102:103]
	v_pk_mul_f32 v[106:107], v[0:1], v[106:107] op_sel_hi:[0,1]
	v_pk_mul_f32 v[98:99], v[98:99], v[102:103]
	v_pk_mul_f32 v[102:103], v[0:1], v[110:111] op_sel_hi:[0,1]
	v_pk_mul_f32 v[102:103], v[44:45], v[102:103]
	v_cvt_pk_bf16_f32 v98, v98, v99
	v_pk_mul_f32 v[102:103], v[112:113], v[102:103]
	v_pk_mul_f32 v[106:107], v[36:37], v[106:107]
	v_cvt_pk_bf16_f32 v99, v102, v103
	v_pk_mul_f32 v[102:103], v[0:1], v[108:109] op_sel_hi:[0,1]
	v_pk_mul_f32 v[102:103], v[34:35], v[102:103]
	s_nop 0
	v_pk_mul_f32 v[102:103], v[104:105], v[102:103]
	s_nop 0
	v_cvt_pk_bf16_f32 v100, v102, v103
	v_lshlrev_b32_e32 v102, 16, v101
	v_and_b32_e32 v103, 0xffff0000, v101
	v_mul_f32_e32 v101, 0xbfb8aa3b, v102
	v_mul_f32_e32 v0, 0xbfb8aa3b, v103
	v_exp_f32_e32 v101, v101
	v_exp_f32_e32 v0, v0
	v_add_f32_e32 v101, 1.0, v101
	v_add_f32_e32 v0, 1.0, v0
	v_rcp_f32_e32 v104, v101
	v_rcp_f32_e32 v105, v0
	s_nop 0
	v_pk_mul_f32 v[102:103], v[104:105], v[102:103]
	s_nop 0
	v_pk_mul_f32 v[102:103], v[102:103], v[106:107]
	s_waitcnt vmcnt(9)
; __device__ __forceinline__ unsigned pk2(float lo, float hi) { const pk_f2 v = {lo, hi}; return __builtin_bit_cast(unsigned, __builtin_convertvector(v, pk_b2)); }
; __device__ __forceinline__ float silu1(float x) { return x * sigmoid_f(x); }
; __device__ __forceinline__ float wave_sum(float v) { v = row16_sum(v); return (WS_RL(v, 0) + WS_RL(v, 16)) + (WS_RL(v, 32) + WS_RL(v, 48)); }
; __device__ __forceinline__ void phase_ret_post(const bf16* O, const bf16* PROJ, const float* ng, bf16* Pb, int gw, int NGW, int lane) {
;     ...
;         for (int hh = 0; hh < 8; ++hh) {
;             const f32x4 o0 = (f32x4){bflo(ob[hh].x), bfhi(ob[hh].x), bflo(ob[hh].y), bfhi(ob[hh].y)}, o1 = (f32x4){bflo(ob[hh].z), bfhi(ob[hh].z), bflo(ob[hh].w), bfhi(ob[hh].w)};
;             const float ss = ((o0.x * o0.x + o0.y * o0.y) + (o0.z * o0.z + o0.w * o0.w)) + ((o1.x * o1.x + o1.y * o1.y) + (o1.z * o1.z + o1.w * o1.w));
;             const float rstd = 1.0f / sqrtf(wave_sum(ss) * (1.0f / 512.0f) + EPS);
;             const v4u g = gq[hh];
;             v4u w; w.x = pk2(o0.x * rstd * nv[hh][0].x * silu1(bflo(g.x)), o0.y * rstd * nv[hh][0].y * silu1(bfhi(g.x))); w.y = pk2(o0.z * rstd * nv[hh][0].z * silu1(bflo(g.y)), o0.w * rstd * nv[hh][0].w * silu1(bfhi(g.y)));
;             w.z = pk2(o1.x * rstd * nv[hh][1].x * silu1(bflo(g.z)), o1.y * rstd * nv[hh][1].y * silu1(bfhi(g.z))); w.w = pk2(o1.z * rstd * nv[hh][1].z * silu1(bflo(g.w)), o1.w * rstd * nv[hh][1].w * silu1(bfhi(g.w)));
;             prow[64 * hh] = w;
	v_lshlrev_b32_e32 v104, 16, v91
	v_cvt_pk_bf16_f32 v101, v102, v103
	global_store_dwordx4 v[132:133], v[98:101], off offset:3072
	v_and_b32_e32 v105, 0xffff0000, v91
	s_nop 0
	v_lshlrev_b32_e32 v100, 16, v96
	v_and_b32_e32 v101, 0xffff0000, v96
	v_lshlrev_b32_e32 v96, 16, v92
	v_mul_f32_e32 v0, 0xbfb8aa3b, v96
	v_exp_f32_e32 v0, v0
	v_lshlrev_b32_e32 v98, 16, v97
	v_and_b32_e32 v99, 0xffff0000, v97
	v_and_b32_e32 v97, 0xffff0000, v92
	v_add_f32_e32 v0, 1.0, v0
	v_rcp_f32_e32 v102, v0
	v_mul_f32_e32 v0, 0xbfb8aa3b, v97
	v_exp_f32_e32 v0, v0
	v_mov_b32_e32 v109, v99
	v_mov_b32_e32 v111, v101
	v_add_f32_e32 v0, 1.0, v0
	v_rcp_f32_e32 v103, v0
	v_mul_f32_e32 v0, 0xbfb8aa3b, v104
	v_exp_f32_e32 v0, v0
	v_pk_mul_f32 v[96:97], v[102:103], v[96:97]
	v_lshlrev_b32_e32 v102, 16, v95
	v_add_f32_e32 v0, 1.0, v0
	v_rcp_f32_e32 v106, v0
	v_mul_f32_e32 v0, 0xbfb8aa3b, v105
	v_exp_f32_e32 v0, v0
	v_and_b32_e32 v103, 0xffff0000, v95
	v_and_b32_e32 v95, 0xffff0000, v90
	v_mov_b32_e32 v108, v103
	v_add_f32_e32 v0, 1.0, v0
	v_rcp_f32_e32 v107, v0
	v_pk_mul_f32 v[108:109], v[108:109], v[108:109]
	v_pk_mul_f32 v[104:105], v[106:107], v[104:105]
	v_lshlrev_b32_e32 v106, 16, v94
	v_and_b32_e32 v107, 0xffff0000, v94
	v_lshlrev_b32_e32 v94, 16, v90
	v_mul_f32_e32 v0, 0xbfb8aa3b, v94
	v_exp_f32_e32 v0, v0
	v_mov_b32_e32 v110, v107
	v_pk_mul_f32 v[110:111], v[110:111], v[110:111]
	v_add_f32_e32 v0, 1.0, v0
	v_rcp_f32_e32 v90, v0
	v_mul_f32_e32 v0, 0xbfb8aa3b, v95
	v_exp_f32_e32 v0, v0
	s_nop 0
	v_add_f32_e32 v0, 1.0, v0
	v_rcp_f32_e32 v91, v0
	s_nop 0
	v_pk_mul_f32 v[90:91], v[90:91], v[94:95]
	v_mov_b32_e32 v94, v102
	v_mov_b32_e32 v95, v98
	v_pk_fma_f32 v[94:95], v[94:95], v[94:95], v[108:109]
	v_mov_b32_e32 v108, v106
	v_mov_b32_e32 v109, v100
	v_pk_fma_f32 v[108:109], v[108:109], v[108:109], v[110:111]
	s_nop 0
	v_pk_add_f32 v[94:95], v[108:109], v[94:95]
	s_nop 0
	v_add_f32_e32 v0, v94, v95
	s_nop 1
	v_add_f32_dpp v0, v0, v0 quad_perm:[1,0,3,2] row_mask:0xf bank_mask:0xf bound_ctrl:1
	s_nop 1
	v_add_f32_dpp v0, v0, v0 quad_perm:[2,3,0,1] row_mask:0xf bank_mask:0xf bound_ctrl:1
	s_nop 1
	v_add_f32_dpp v0, v0, v0 row_half_mirror row_mask:0xf bank_mask:0xf bound_ctrl:1
	s_nop 1
	v_add_f32_dpp v0, v0, v0 row_mirror row_mask:0xf bank_mask:0xf bound_ctrl:1
	s_nop 0
	v_readlane_b32 s1, v0, 16
	v_readlane_b32 s4, v0, 48
	v_readlane_b32 s2, v0, 0
	v_readlane_b32 s3, v0, 32
	v_mov_b32_e32 v94, s1
	v_mov_b32_e32 v95, s4
	v_pk_add_f32 v[94:95], s[2:3], v[94:95]
	s_nop 0
	v_add_f32_e32 v0, v94, v95
	v_fmamk_f32 v0, v0, 0x3b000000, v192
	v_rsq_f32_e32 v92, v0
	s_nop 0
	v_mul_f32_e32 v94, v0, v92
	v_fma_f32 v94, -v94, v92, 1.0
	v_mul_f32_e32 v95, 0.5, v92
	v_fma_f32 v0, v95, v94, v92
	v_pk_mul_f32 v[94:95], v[0:1], v[106:107] op_sel_hi:[0,1]
	v_pk_mul_f32 v[94:95], v[22:23], v[94:95]
	v_pk_mul_f32 v[98:99], v[0:1], v[98:99] op_sel_hi:[0,1]
	v_pk_mul_f32 v[90:91], v[90:91], v[94:95]
	v_pk_mul_f32 v[94:95], v[0:1], v[102:103] op_sel_hi:[0,1]
	v_pk_mul_f32 v[94:95], v[24:25], v[94:95]
	v_cvt_pk_bf16_f32 v90, v90, v91
	v_pk_mul_f32 v[94:95], v[104:105], v[94:95]
	v_pk_mul_f32 v[98:99], v[32:33], v[98:99]
	v_cvt_pk_bf16_f32 v91, v94, v95
	v_pk_mul_f32 v[94:95], v[0:1], v[100:101] op_sel_hi:[0,1]
	v_pk_mul_f32 v[94:95], v[30:31], v[94:95]
	s_nop 0
	v_pk_mul_f32 v[94:95], v[96:97], v[94:95]
	s_nop 0
	v_cvt_pk_bf16_f32 v92, v94, v95
	v_lshlrev_b32_e32 v94, 16, v93
	v_and_b32_e32 v95, 0xffff0000, v93
	v_mul_f32_e32 v93, 0xbfb8aa3b, v94
	v_mul_f32_e32 v0, 0xbfb8aa3b, v95
	v_exp_f32_e32 v93, v93
	v_exp_f32_e32 v0, v0
	v_add_f32_e32 v93, 1.0, v93
	v_add_f32_e32 v0, 1.0, v0
	v_rcp_f32_e32 v96, v93
	v_rcp_f32_e32 v97, v0
	s_nop 0
	v_pk_mul_f32 v[94:95], v[96:97], v[94:95]
	s_nop 0
	v_pk_mul_f32 v[94:95], v[94:95], v[98:99]
	s_waitcnt vmcnt(8)
	v_lshlrev_b32_e32 v96, 16, v83
	v_cvt_pk_bf16_f32 v93, v94, v95
	global_store_dwordx4 v[130:131], v[90:93], off
	v_and_b32_e32 v97, 0xffff0000, v83
	s_nop 0
	v_lshlrev_b32_e32 v92, 16, v88
	v_and_b32_e32 v93, 0xffff0000, v88
	v_lshlrev_b32_e32 v88, 16, v84
	v_mul_f32_e32 v0, 0xbfb8aa3b, v88
	v_exp_f32_e32 v0, v0
	v_lshlrev_b32_e32 v90, 16, v89
	v_and_b32_e32 v91, 0xffff0000, v89
	v_and_b32_e32 v89, 0xffff0000, v84
	v_add_f32_e32 v0, 1.0, v0
	v_rcp_f32_e32 v94, v0
	v_mul_f32_e32 v0, 0xbfb8aa3b, v89
	v_exp_f32_e32 v0, v0
	v_mov_b32_e32 v101, v91
	v_mov_b32_e32 v103, v93
	v_add_f32_e32 v0, 1.0, v0
	v_rcp_f32_e32 v95, v0
	v_mul_f32_e32 v0, 0xbfb8aa3b, v96
	v_exp_f32_e32 v0, v0
	v_pk_mul_f32 v[88:89], v[94:95], v[88:89]
	v_lshlrev_b32_e32 v94, 16, v87
	v_add_f32_e32 v0, 1.0, v0
	v_rcp_f32_e32 v98, v0
	v_mul_f32_e32 v0, 0xbfb8aa3b, v97
	v_exp_f32_e32 v0, v0
	v_and_b32_e32 v95, 0xffff0000, v87
	v_and_b32_e32 v87, 0xffff0000, v82
	v_mov_b32_e32 v100, v95
	v_add_f32_e32 v0, 1.0, v0
	v_rcp_f32_e32 v99, v0
	v_pk_mul_f32 v[100:101], v[100:101], v[100:101]
	v_pk_mul_f32 v[96:97], v[98:99], v[96:97]
	v_lshlrev_b32_e32 v98, 16, v86
	v_and_b32_e32 v99, 0xffff0000, v86
	v_lshlrev_b32_e32 v86, 16, v82
	v_mul_f32_e32 v0, 0xbfb8aa3b, v86
	v_exp_f32_e32 v0, v0
	v_mov_b32_e32 v102, v99
	v_pk_mul_f32 v[102:103], v[102:103], v[102:103]
	v_add_f32_e32 v0, 1.0, v0
	v_rcp_f32_e32 v82, v0
	v_mul_f32_e32 v0, 0xbfb8aa3b, v87
	v_exp_f32_e32 v0, v0
	s_nop 0
	v_add_f32_e32 v0, 1.0, v0
	v_rcp_f32_e32 v83, v0
	s_nop 0
	v_pk_mul_f32 v[82:83], v[82:83], v[86:87]
	v_mov_b32_e32 v86, v94
	v_mov_b32_e32 v87, v90
	v_pk_fma_f32 v[86:87], v[86:87], v[86:87], v[100:101]
	v_mov_b32_e32 v100, v98
	v_mov_b32_e32 v101, v92
	v_pk_fma_f32 v[100:101], v[100:101], v[100:101], v[102:103]
	s_nop 0
	v_pk_add_f32 v[86:87], v[100:101], v[86:87]
	s_nop 0
	v_add_f32_e32 v0, v86, v87
	s_nop 1
; __device__ __forceinline__ unsigned pk2(float lo, float hi) { const pk_f2 v = {lo, hi}; return __builtin_bit_cast(unsigned, __builtin_convertvector(v, pk_b2)); }
; __device__ __forceinline__ float silu1(float x) { return x * sigmoid_f(x); }
; __device__ __forceinline__ float wave_sum(float v) { v = row16_sum(v); return (WS_RL(v, 0) + WS_RL(v, 16)) + (WS_RL(v, 32) + WS_RL(v, 48)); }
; __device__ __forceinline__ void phase_ret_post(const bf16* O, const bf16* PROJ, const float* ng, bf16* Pb, int gw, int NGW, int lane) {
;     ...
;         for (int hh = 0; hh < 8; ++hh) {
;             const f32x4 o0 = (f32x4){bflo(ob[hh].x), bfhi(ob[hh].x), bflo(ob[hh].y), bfhi(ob[hh].y)}, o1 = (f32x4){bflo(ob[hh].z), bfhi(ob[hh].z), bflo(ob[hh].w), bfhi(ob[hh].w)};
;             const float ss = ((o0.x * o0.x + o0.y * o0.y) + (o0.z * o0.z + o0.w * o0.w)) + ((o1.x * o1.x + o1.y * o1.y) + (o1.z * o1.z + o1.w * o1.w));
;             const float rstd = 1.0f / sqrtf(wave_sum(ss) * (1.0f / 512.0f) + EPS);
;             const v4u g = gq[hh];
;             v4u w; w.x = pk2(o0.x * rstd * nv[hh][0].x * silu1(bflo(g.x)), o0.y * rstd * nv[hh][0].y * silu1(bfhi(g.x))); w.y = pk2(o0.z * rstd * nv[hh][0].z * silu1(bflo(g.y)), o0.w * rstd * nv[hh][0].w * silu1(bfhi(g.y)));
;             w.z = pk2(o1.x * rstd * nv[hh][1].x * silu1(bflo(g.z)), o1.y * rstd * nv[hh][1].y * silu1(bfhi(g.z))); w.w = pk2(o1.z * rstd * nv[hh][1].z * silu1(bflo(g.w)), o1.w * rstd * nv[hh][1].w * silu1(bfhi(g.w)));
;             prow[64 * hh] = w;
	v_add_f32_dpp v0, v0, v0 quad_perm:[1,0,3,2] row_mask:0xf bank_mask:0xf bound_ctrl:1
	s_nop 1
	v_add_f32_dpp v0, v0, v0 quad_perm:[2,3,0,1] row_mask:0xf bank_mask:0xf bound_ctrl:1
	s_nop 1
	v_add_f32_dpp v0, v0, v0 row_half_mirror row_mask:0xf bank_mask:0xf bound_ctrl:1
	s_nop 1
	v_add_f32_dpp v0, v0, v0 row_mirror row_mask:0xf bank_mask:0xf bound_ctrl:1
	s_nop 0
	v_readlane_b32 s1, v0, 16
	v_readlane_b32 s4, v0, 48
	v_readlane_b32 s2, v0, 0
	v_readlane_b32 s3, v0, 32
	v_mov_b32_e32 v86, s1
	v_mov_b32_e32 v87, s4
	v_pk_add_f32 v[86:87], s[2:3], v[86:87]
	s_nop 0
	v_add_f32_e32 v0, v86, v87
	v_fmamk_f32 v0, v0, 0x3b000000, v192
	v_rsq_f32_e32 v84, v0
	s_nop 0
	v_mul_f32_e32 v86, v0, v84
	v_fma_f32 v86, -v86, v84, 1.0
	v_mul_f32_e32 v87, 0.5, v84
	v_fma_f32 v0, v87, v86, v84
	v_pk_mul_f32 v[86:87], v[0:1], v[98:99] op_sel_hi:[0,1]
	v_pk_mul_f32 v[86:87], v[26:27], v[86:87]
	v_pk_mul_f32 v[90:91], v[0:1], v[90:91] op_sel_hi:[0,1]
	v_pk_mul_f32 v[82:83], v[82:83], v[86:87]
	v_pk_mul_f32 v[86:87], v[0:1], v[94:95] op_sel_hi:[0,1]
	v_pk_mul_f32 v[86:87], v[28:29], v[86:87]
	v_cvt_pk_bf16_f32 v82, v82, v83
	v_pk_mul_f32 v[86:87], v[96:97], v[86:87]
	v_pk_mul_f32 v[90:91], v[20:21], v[90:91]
	v_cvt_pk_bf16_f32 v83, v86, v87
	v_pk_mul_f32 v[86:87], v[0:1], v[92:93] op_sel_hi:[0,1]
	v_pk_mul_f32 v[86:87], v[18:19], v[86:87]
	s_nop 0
	v_pk_mul_f32 v[86:87], v[88:89], v[86:87]
	s_nop 0
	v_cvt_pk_bf16_f32 v84, v86, v87
	v_lshlrev_b32_e32 v86, 16, v85
	v_and_b32_e32 v87, 0xffff0000, v85
	v_mul_f32_e32 v85, 0xbfb8aa3b, v86
	v_mul_f32_e32 v0, 0xbfb8aa3b, v87
	v_exp_f32_e32 v85, v85
	v_exp_f32_e32 v0, v0
	v_add_f32_e32 v85, 1.0, v85
	v_add_f32_e32 v0, 1.0, v0
	v_rcp_f32_e32 v88, v85
	v_rcp_f32_e32 v89, v0
	s_nop 0
	v_pk_mul_f32 v[86:87], v[88:89], v[86:87]
	s_nop 0
	v_pk_mul_f32 v[86:87], v[86:87], v[90:91]
	s_waitcnt vmcnt(7)
	v_lshlrev_b32_e32 v88, 16, v75
	v_cvt_pk_bf16_f32 v85, v86, v87
	global_store_dwordx4 v[130:131], v[82:85], off offset:1024
	v_and_b32_e32 v89, 0xffff0000, v75
	s_nop 0
	v_lshlrev_b32_e32 v84, 16, v80
	v_and_b32_e32 v85, 0xffff0000, v80
	v_lshlrev_b32_e32 v80, 16, v76
	v_mul_f32_e32 v0, 0xbfb8aa3b, v80
	v_exp_f32_e32 v0, v0
	v_lshlrev_b32_e32 v82, 16, v81
	v_and_b32_e32 v83, 0xffff0000, v81
	v_and_b32_e32 v81, 0xffff0000, v76
	v_add_f32_e32 v0, 1.0, v0
	v_rcp_f32_e32 v86, v0
	v_mul_f32_e32 v0, 0xbfb8aa3b, v81
	v_exp_f32_e32 v0, v0
	v_mov_b32_e32 v93, v83
	v_mov_b32_e32 v95, v85
	v_add_f32_e32 v0, 1.0, v0
	v_rcp_f32_e32 v87, v0
	v_mul_f32_e32 v0, 0xbfb8aa3b, v88
	v_exp_f32_e32 v0, v0
	v_pk_mul_f32 v[80:81], v[86:87], v[80:81]
	v_lshlrev_b32_e32 v86, 16, v79
	v_add_f32_e32 v0, 1.0, v0
	v_rcp_f32_e32 v90, v0
	v_mul_f32_e32 v0, 0xbfb8aa3b, v89
	v_exp_f32_e32 v0, v0
	v_and_b32_e32 v87, 0xffff0000, v79
	v_and_b32_e32 v79, 0xffff0000, v74
	v_mov_b32_e32 v92, v87
	v_add_f32_e32 v0, 1.0, v0
	v_rcp_f32_e32 v91, v0
	v_pk_mul_f32 v[92:93], v[92:93], v[92:93]
	v_pk_mul_f32 v[88:89], v[90:91], v[88:89]
	v_lshlrev_b32_e32 v90, 16, v78
	v_and_b32_e32 v91, 0xffff0000, v78
	v_lshlrev_b32_e32 v78, 16, v74
	v_mul_f32_e32 v0, 0xbfb8aa3b, v78
	v_exp_f32_e32 v0, v0
	v_mov_b32_e32 v94, v91
	v_pk_mul_f32 v[94:95], v[94:95], v[94:95]
	v_add_f32_e32 v0, 1.0, v0
	v_rcp_f32_e32 v74, v0
	v_mul_f32_e32 v0, 0xbfb8aa3b, v79
	v_exp_f32_e32 v0, v0
	s_nop 0
	v_add_f32_e32 v0, 1.0, v0
	v_rcp_f32_e32 v75, v0
	s_nop 0
	v_pk_mul_f32 v[74:75], v[74:75], v[78:79]
	v_mov_b32_e32 v78, v86
	v_mov_b32_e32 v79, v82
	v_pk_fma_f32 v[78:79], v[78:79], v[78:79], v[92:93]
	v_mov_b32_e32 v92, v90
	v_mov_b32_e32 v93, v84
	v_pk_fma_f32 v[92:93], v[92:93], v[92:93], v[94:95]
	s_nop 0
	v_pk_add_f32 v[78:79], v[92:93], v[78:79]
	s_nop 0
	v_add_f32_e32 v0, v78, v79
	s_nop 1
	v_add_f32_dpp v0, v0, v0 quad_perm:[1,0,3,2] row_mask:0xf bank_mask:0xf bound_ctrl:1
	s_nop 1
	v_add_f32_dpp v0, v0, v0 quad_perm:[2,3,0,1] row_mask:0xf bank_mask:0xf bound_ctrl:1
	s_nop 1
	v_add_f32_dpp v0, v0, v0 row_half_mirror row_mask:0xf bank_mask:0xf bound_ctrl:1
	s_nop 1
	v_add_f32_dpp v0, v0, v0 row_mirror row_mask:0xf bank_mask:0xf bound_ctrl:1
	s_nop 0
	v_readlane_b32 s1, v0, 16
	v_readlane_b32 s4, v0, 48
	v_readlane_b32 s2, v0, 0
	v_readlane_b32 s3, v0, 32
	v_mov_b32_e32 v78, s1
	v_mov_b32_e32 v79, s4
	v_pk_add_f32 v[78:79], s[2:3], v[78:79]
	s_nop 0
	v_add_f32_e32 v0, v78, v79
	v_fmamk_f32 v0, v0, 0x3b000000, v192
	v_rsq_f32_e32 v76, v0
	s_nop 0
	v_mul_f32_e32 v78, v0, v76
	v_fma_f32 v78, -v78, v76, 1.0
	v_mul_f32_e32 v79, 0.5, v76
	v_fma_f32 v0, v79, v78, v76
	v_pk_mul_f32 v[78:79], v[0:1], v[90:91] op_sel_hi:[0,1]
	v_pk_mul_f32 v[78:79], v[6:7], v[78:79]
	v_pk_mul_f32 v[82:83], v[0:1], v[82:83] op_sel_hi:[0,1]
	v_pk_mul_f32 v[74:75], v[74:75], v[78:79]
	v_pk_mul_f32 v[78:79], v[0:1], v[86:87] op_sel_hi:[0,1]
	v_pk_mul_f32 v[78:79], v[8:9], v[78:79]
	v_cvt_pk_bf16_f32 v74, v74, v75
	v_pk_mul_f32 v[78:79], v[88:89], v[78:79]
	v_pk_mul_f32 v[82:83], v[16:17], v[82:83]
	v_cvt_pk_bf16_f32 v75, v78, v79
	v_pk_mul_f32 v[78:79], v[0:1], v[84:85] op_sel_hi:[0,1]
	v_pk_mul_f32 v[78:79], v[14:15], v[78:79]
	s_nop 0
	v_pk_mul_f32 v[78:79], v[80:81], v[78:79]
	s_nop 0
	v_cvt_pk_bf16_f32 v76, v78, v79
	v_lshlrev_b32_e32 v78, 16, v77
	v_and_b32_e32 v79, 0xffff0000, v77
	v_mul_f32_e32 v77, 0xbfb8aa3b, v78
	v_mul_f32_e32 v0, 0xbfb8aa3b, v79
	v_exp_f32_e32 v77, v77
	v_exp_f32_e32 v0, v0
	v_add_f32_e32 v77, 1.0, v77
	v_add_f32_e32 v0, 1.0, v0
	v_rcp_f32_e32 v80, v77
	v_rcp_f32_e32 v81, v0
	s_nop 0
	v_pk_mul_f32 v[78:79], v[80:81], v[78:79]
	s_nop 0
	v_pk_mul_f32 v[78:79], v[78:79], v[82:83]
	s_waitcnt vmcnt(6)
; #define GAS __attribute__((address_space(1)))
; __device__ __forceinline__ unsigned pk2(float lo, float hi) { const pk_f2 v = {lo, hi}; return __builtin_bit_cast(unsigned, __builtin_convertvector(v, pk_b2)); }
; __device__ __forceinline__ float silu1(float x) { return x * sigmoid_f(x); }
; __device__ __forceinline__ float wave_sum(float v) { v = row16_sum(v); return (WS_RL(v, 0) + WS_RL(v, 16)) + (WS_RL(v, 32) + WS_RL(v, 48)); }
; __device__ __forceinline__ void phase_ret_post(const bf16* O, const bf16* PROJ, const float* ng, bf16* Pb, int gw, int NGW, int lane) {
;     ...
;     for (int m = gw; m < M; m += NGW) {
;         const GAS v4u* orow = (const GAS v4u*)(O + (size_t)m * RT_V) + lane;
;         const GAS v4u* grow = (const GAS v4u*)(PROJ + (size_t)m * RT_IN + 8192) + lane;
;         GAS v4u* prow = (GAS v4u*)(Pb + (size_t)m * RT_V) + lane;
;         v4u ob[8], gq[8];
; #pragma unroll
;         for (int hh = 0; hh < 8; ++hh) { ob[hh] = orow[64 * hh]; gq[hh] = grow[64 * hh]; }
; #pragma unroll
;         for (int hh = 0; hh < 8; ++hh) {
;             const f32x4 o0 = (f32x4){bflo(ob[hh].x), bfhi(ob[hh].x), bflo(ob[hh].y), bfhi(ob[hh].y)}, o1 = (f32x4){bflo(ob[hh].z), bfhi(ob[hh].z), bflo(ob[hh].w), bfhi(ob[hh].w)};
;             const float ss = ((o0.x * o0.x + o0.y * o0.y) + (o0.z * o0.z + o0.w * o0.w)) + ((o1.x * o1.x + o1.y * o1.y) + (o1.z * o1.z + o1.w * o1.w));
;             const float rstd = 1.0f / sqrtf(wave_sum(ss) * (1.0f / 512.0f) + EPS);
;             const v4u g = gq[hh];
;             v4u w; w.x = pk2(o0.x * rstd * nv[hh][0].x * silu1(bflo(g.x)), o0.y * rstd * nv[hh][0].y * silu1(bfhi(g.x))); w.y = pk2(o0.z * rstd * nv[hh][0].z * silu1(bflo(g.y)), o0.w * rstd * nv[hh][0].w * silu1(bfhi(g.y)));
;             w.z = pk2(o1.x * rstd * nv[hh][1].x * silu1(bflo(g.z)), o1.y * rstd * nv[hh][1].y * silu1(bfhi(g.z))); w.w = pk2(o1.z * rstd * nv[hh][1].z * silu1(bflo(g.w)), o1.w * rstd * nv[hh][1].w * silu1(bfhi(g.w)));
;             prow[64 * hh] = w;
;         }
;     }
	v_lshlrev_b32_e32 v80, 16, v67
	v_cvt_pk_bf16_f32 v77, v78, v79
	global_store_dwordx4 v[130:131], v[74:77], off offset:2048
	v_and_b32_e32 v81, 0xffff0000, v67
	s_nop 0
	v_lshlrev_b32_e32 v76, 16, v72
	v_and_b32_e32 v77, 0xffff0000, v72
	v_lshlrev_b32_e32 v72, 16, v68
	v_mul_f32_e32 v0, 0xbfb8aa3b, v72
	v_exp_f32_e32 v0, v0
	v_lshlrev_b32_e32 v74, 16, v73
	v_and_b32_e32 v75, 0xffff0000, v73
	v_and_b32_e32 v73, 0xffff0000, v68
	v_add_f32_e32 v0, 1.0, v0
	v_rcp_f32_e32 v78, v0
	v_mul_f32_e32 v0, 0xbfb8aa3b, v73
	v_exp_f32_e32 v0, v0
	v_mov_b32_e32 v85, v75
	v_mov_b32_e32 v87, v77
	v_add_f32_e32 v0, 1.0, v0
	v_rcp_f32_e32 v79, v0
	v_mul_f32_e32 v0, 0xbfb8aa3b, v80
	v_exp_f32_e32 v0, v0
	v_pk_mul_f32 v[72:73], v[78:79], v[72:73]
	v_lshlrev_b32_e32 v78, 16, v71
	v_add_f32_e32 v0, 1.0, v0
	v_rcp_f32_e32 v82, v0
	v_mul_f32_e32 v0, 0xbfb8aa3b, v81
	v_exp_f32_e32 v0, v0
	v_and_b32_e32 v79, 0xffff0000, v71
	v_and_b32_e32 v71, 0xffff0000, v66
	v_mov_b32_e32 v84, v79
	v_add_f32_e32 v0, 1.0, v0
	v_rcp_f32_e32 v83, v0
	v_pk_mul_f32 v[84:85], v[84:85], v[84:85]
	v_pk_mul_f32 v[80:81], v[82:83], v[80:81]
	v_lshlrev_b32_e32 v82, 16, v70
	v_and_b32_e32 v83, 0xffff0000, v70
	v_lshlrev_b32_e32 v70, 16, v66
	v_mul_f32_e32 v0, 0xbfb8aa3b, v70
	v_exp_f32_e32 v0, v0
	v_mov_b32_e32 v86, v83
	v_pk_mul_f32 v[86:87], v[86:87], v[86:87]
	v_add_f32_e32 v0, 1.0, v0
	v_rcp_f32_e32 v66, v0
	v_mul_f32_e32 v0, 0xbfb8aa3b, v71
	v_exp_f32_e32 v0, v0
	s_nop 0
	v_add_f32_e32 v0, 1.0, v0
	v_rcp_f32_e32 v67, v0
	s_nop 0
	v_pk_mul_f32 v[66:67], v[66:67], v[70:71]
	v_mov_b32_e32 v70, v78
	v_mov_b32_e32 v71, v74
	v_pk_fma_f32 v[70:71], v[70:71], v[70:71], v[84:85]
	v_mov_b32_e32 v84, v82
	v_mov_b32_e32 v85, v76
	v_pk_fma_f32 v[84:85], v[84:85], v[84:85], v[86:87]
	s_nop 0
	v_pk_add_f32 v[70:71], v[84:85], v[70:71]
	s_nop 0
	v_add_f32_e32 v0, v70, v71
	s_nop 1
	v_add_f32_dpp v0, v0, v0 quad_perm:[1,0,3,2] row_mask:0xf bank_mask:0xf bound_ctrl:1
	s_nop 1
	v_add_f32_dpp v0, v0, v0 quad_perm:[2,3,0,1] row_mask:0xf bank_mask:0xf bound_ctrl:1
	s_nop 1
	v_add_f32_dpp v0, v0, v0 row_half_mirror row_mask:0xf bank_mask:0xf bound_ctrl:1
	s_nop 1
	v_add_f32_dpp v0, v0, v0 row_mirror row_mask:0xf bank_mask:0xf bound_ctrl:1
	s_nop 0
	v_readlane_b32 s1, v0, 16
	v_readlane_b32 s4, v0, 48
	v_readlane_b32 s2, v0, 0
	v_readlane_b32 s3, v0, 32
	v_mov_b32_e32 v70, s1
	v_mov_b32_e32 v71, s4
	v_pk_add_f32 v[70:71], s[2:3], v[70:71]
	s_mul_i32 s1, s58, 0x6000
	v_add_f32_e32 v0, v70, v71
	v_fmamk_f32 v0, v0, 0x3b000000, v192
	v_rsq_f32_e32 v68, v0
	s_nop 0
	v_mul_f32_e32 v70, v0, v68
	v_fma_f32 v70, -v70, v68, 1.0
	v_mul_f32_e32 v71, 0.5, v68
	v_fma_f32 v0, v71, v70, v68
	s_add_u32 s18, s18, s1
	s_mul_hi_i32 s1, s58, 0x6000
	s_addc_u32 s19, s19, s1
	s_add_u32 s44, s44, s8
	s_addc_u32 s45, s45, s9
	s_cmpk_lt_i32 s0, 0x4000
	v_pk_mul_f32 v[70:71], v[0:1], v[82:83] op_sel_hi:[0,1]
	v_pk_mul_f32 v[70:71], v[10:11], v[70:71]
	v_pk_mul_f32 v[74:75], v[0:1], v[74:75] op_sel_hi:[0,1]
	v_pk_mul_f32 v[66:67], v[66:67], v[70:71]
	v_pk_mul_f32 v[70:71], v[0:1], v[78:79] op_sel_hi:[0,1]
	v_pk_mul_f32 v[70:71], v[12:13], v[70:71]
	v_cvt_pk_bf16_f32 v66, v66, v67
	v_pk_mul_f32 v[70:71], v[80:81], v[70:71]
	v_pk_mul_f32 v[74:75], v[4:5], v[74:75]
	v_cvt_pk_bf16_f32 v67, v70, v71
	v_pk_mul_f32 v[70:71], v[0:1], v[76:77] op_sel_hi:[0,1]
	v_pk_mul_f32 v[70:71], v[2:3], v[70:71]
	s_nop 0
	v_pk_mul_f32 v[70:71], v[72:73], v[70:71]
	s_nop 0
	v_cvt_pk_bf16_f32 v68, v70, v71
	v_lshlrev_b32_e32 v70, 16, v69
	v_and_b32_e32 v71, 0xffff0000, v69
	v_mul_f32_e32 v69, 0xbfb8aa3b, v70
	v_mul_f32_e32 v0, 0xbfb8aa3b, v71
	v_exp_f32_e32 v69, v69
	v_exp_f32_e32 v0, v0
	v_add_f32_e32 v69, 1.0, v69
	v_add_f32_e32 v0, 1.0, v0
	v_rcp_f32_e32 v72, v69
	v_rcp_f32_e32 v73, v0
	s_nop 0
	v_pk_mul_f32 v[70:71], v[72:73], v[70:71]
	s_nop 0
	v_pk_mul_f32 v[70:71], v[70:71], v[74:75]
	s_nop 0
	v_cvt_pk_bf16_f32 v69, v70, v71
	global_store_dwordx4 v[130:131], v[66:69], off offset:3072
	s_cbranch_scc1 .LBB0_856

; #define GAS __attribute__((address_space(1)))
; __device__ __forceinline__ unsigned pk2(float lo, float hi) { const pk_f2 v = {lo, hi}; return __builtin_bit_cast(unsigned, __builtin_convertvector(v, pk_b2)); }
; __device__ __forceinline__ float silu1(float x) { return x * sigmoid_f(x); }
; __device__ __forceinline__ float row16_sum(float v) { v += WS_DPP(v, 0xB1); v += WS_DPP(v, 0x4E); v += WS_DPP(v, 0x141); v += WS_DPP(v, 0x140); return v; }
; __device__ __forceinline__ void phase_hgrn_post(const bf16* O, const bf16* PROJ, const float* ng, bf16* Pb, int gw, int NGW, int lane) {
;     ...
;     for (int m = gw; m < M; m += NGW) {
;         const GAS v4u* orow = (const GAS v4u*)(O + (size_t)m * DM) + lane;
;         const GAS v4u* grow = (const GAS v4u*)(PROJ + (size_t)m * HG_IN + 6144) + lane;
;         GAS v4u* prow = (GAS v4u*)(Pb + (size_t)m * DM) + lane;
;         v4u ob[4], gq[4];
; #pragma unroll
;         for (int j = 0; j < 4; ++j) { ob[j] = orow[64 * j]; gq[j] = grow[64 * j]; }
; #pragma unroll
;         for (int j = 0; j < 4; ++j) {
;             const f32x4 o0 = (f32x4){bflo(ob[j].x), bfhi(ob[j].x), bflo(ob[j].y), bfhi(ob[j].y)}, o1 = (f32x4){bflo(ob[j].z), bfhi(ob[j].z), bflo(ob[j].w), bfhi(ob[j].w)};
;             float ss = ((o0.x * o0.x + o0.y * o0.y) + (o0.z * o0.z + o0.w * o0.w)) + ((o1.x * o1.x + o1.y * o1.y) + (o1.z * o1.z + o1.w * o1.w));
;             ss = row16_sum(ss);
;             const float rstd = 1.0f / sqrtf(ss * (1.0f / 128.0f) + EPS);
;             const v4u g = gq[j];
;             v4u w; w.x = pk2(o0.x * rstd * nv[j][0].x * silu1(bflo(g.x)), o0.y * rstd * nv[j][0].y * silu1(bfhi(g.x))); w.y = pk2(o0.z * rstd * nv[j][0].z * silu1(bflo(g.y)), o0.w * rstd * nv[j][0].w * silu1(bfhi(g.y)));
;             w.z = pk2(o1.x * rstd * nv[j][1].x * silu1(bflo(g.z)), o1.y * rstd * nv[j][1].y * silu1(bfhi(g.z))); w.w = pk2(o1.z * rstd * nv[j][1].z * silu1(bflo(g.w)), o1.w * rstd * nv[j][1].w * silu1(bfhi(g.w)));
.LBB0_861:
	v_lshl_add_u64 v[68:69], s[12:13], 0, v[50:51]
	v_add_co_u32_e32 v36, vcc, 0x3c800000, v68
	v_lshl_add_u64 v[34:35], s[0:1], 0, v[50:51]
	s_nop 0
	v_addc_co_u32_e32 v37, vcc, 0, v69, vcc
	global_load_dwordx4 v[52:55], v[36:37], off
	v_add_co_u32_e32 v34, vcc, 0x24803000, v34
	s_add_i32 s2, s2, s58
	s_nop 0
	v_addc_co_u32_e32 v35, vcc, 0, v35, vcc
	global_load_dwordx4 v[56:59], v[34:35], off
	global_load_dwordx4 v[60:63], v[36:37], off offset:1024
	global_load_dwordx4 v[64:67], v[34:35], off offset:1024
	global_load_dwordx4 v[46:49], v[36:37], off offset:2048
	global_load_dwordx4 v[42:45], v[34:35], off offset:2048
	global_load_dwordx4 v[38:41], v[36:37], off offset:3072
	s_nop 0
	global_load_dwordx4 v[34:37], v[34:35], off offset:3072
	s_add_u32 s0, s0, s8
	s_addc_u32 s1, s1, s9
	s_add_u32 s12, s12, s14
	s_addc_u32 s13, s13, s15
	s_cmpk_gt_i32 s2, 0x3fff
	s_waitcnt vmcnt(7)
	v_lshlrev_b32_e32 v72, 16, v54
	v_and_b32_e32 v73, 0xffff0000, v54
	s_waitcnt vmcnt(6)
	v_lshlrev_b32_e32 v54, 16, v58
	v_mul_f32_e32 v0, 0xbfb8aa3b, v54
	v_exp_f32_e32 v0, v0
	v_lshlrev_b32_e32 v70, 16, v55
	v_and_b32_e32 v71, 0xffff0000, v55
	v_and_b32_e32 v55, 0xffff0000, v58
	v_add_f32_e32 v0, 1.0, v0
	v_rcp_f32_e32 v74, v0
	v_mul_f32_e32 v0, 0xbfb8aa3b, v55
	v_exp_f32_e32 v0, v0
	v_lshlrev_b32_e32 v76, 16, v53
	v_and_b32_e32 v77, 0xffff0000, v53
	v_and_b32_e32 v53, 0xffff0000, v56
	v_add_f32_e32 v0, 1.0, v0
	v_rcp_f32_e32 v75, v0
	v_mov_b32_e32 v80, v77
	v_mov_b32_e32 v81, v71
	v_pk_mul_f32 v[80:81], v[80:81], v[80:81]
	v_pk_mul_f32 v[74:75], v[74:75], v[54:55]
	v_lshlrev_b32_e32 v54, 16, v57
	v_mul_f32_e32 v0, 0xbfb8aa3b, v54
	v_exp_f32_e32 v0, v0
	v_and_b32_e32 v55, 0xffff0000, v57
	v_mov_b32_e32 v83, v73
	v_add_f32_e32 v0, 1.0, v0
	v_rcp_f32_e32 v78, v0
	v_mul_f32_e32 v0, 0xbfb8aa3b, v55
	v_exp_f32_e32 v0, v0
	s_nop 0
	v_add_f32_e32 v0, 1.0, v0
	v_rcp_f32_e32 v79, v0
	s_nop 0
	v_pk_mul_f32 v[78:79], v[78:79], v[54:55]
	v_lshlrev_b32_e32 v54, 16, v52
	v_and_b32_e32 v55, 0xffff0000, v52
	v_lshlrev_b32_e32 v52, 16, v56
	v_mul_f32_e32 v0, 0xbfb8aa3b, v52
	v_exp_f32_e32 v0, v0
	v_mov_b32_e32 v82, v55
	v_pk_mul_f32 v[82:83], v[82:83], v[82:83]
	v_add_f32_e32 v0, 1.0, v0
	v_rcp_f32_e32 v56, v0
	v_mul_f32_e32 v0, 0xbfb8aa3b, v53
	v_exp_f32_e32 v0, v0
	s_nop 0
	v_add_f32_e32 v0, 1.0, v0
	v_rcp_f32_e32 v57, v0
	s_nop 0
	v_pk_mul_f32 v[52:53], v[56:57], v[52:53]
	v_mov_b32_e32 v56, v76
	v_mov_b32_e32 v57, v70
	v_pk_fma_f32 v[56:57], v[56:57], v[56:57], v[80:81]
	v_mov_b32_e32 v80, v54
	v_mov_b32_e32 v81, v72
	v_pk_fma_f32 v[80:81], v[80:81], v[80:81], v[82:83]
	s_nop 0
	v_pk_add_f32 v[56:57], v[80:81], v[56:57]
	s_nop 0
	v_add_f32_e32 v0, v56, v57
	s_nop 1
	v_add_f32_dpp v0, v0, v0 quad_perm:[1,0,3,2] row_mask:0xf bank_mask:0xf bound_ctrl:1
	s_nop 1
	v_add_f32_dpp v0, v0, v0 quad_perm:[2,3,0,1] row_mask:0xf bank_mask:0xf bound_ctrl:1
	s_nop 1
	v_add_f32_dpp v0, v0, v0 row_half_mirror row_mask:0xf bank_mask:0xf bound_ctrl:1
	s_nop 1
	v_add_f32_dpp v0, v0, v0 row_mirror row_mask:0xf bank_mask:0xf bound_ctrl:1
	v_fmamk_f32 v0, v0, 0x3c000000, v192
	v_rsq_f32_e32 v56, v0
	s_nop 0
	v_mul_f32_e32 v57, v0, v56
	v_fma_f32 v57, -v57, v56, 1.0
	v_mul_f32_e32 v58, 0.5, v56
	v_fma_f32 v0, v58, v57, v56
	v_pk_mul_f32 v[54:55], v[0:1], v[54:55] op_sel_hi:[0,1]
	v_pk_mul_f32 v[54:55], v[26:27], v[54:55]
	v_pk_mul_f32 v[70:71], v[0:1], v[70:71] op_sel_hi:[0,1]
	v_pk_mul_f32 v[52:53], v[52:53], v[54:55]
	v_pk_mul_f32 v[70:71], v[32:33], v[70:71]
	v_cvt_pk_bf16_f32 v54, v52, v53
	v_pk_mul_f32 v[52:53], v[0:1], v[76:77] op_sel_hi:[0,1]
	v_pk_mul_f32 v[52:53], v[28:29], v[52:53]
	s_nop 0
	v_pk_mul_f32 v[52:53], v[78:79], v[52:53]
	s_nop 0
	v_cvt_pk_bf16_f32 v55, v52, v53
	v_pk_mul_f32 v[52:53], v[0:1], v[72:73] op_sel_hi:[0,1]
	v_pk_mul_f32 v[52:53], v[30:31], v[52:53]
	s_nop 0
	v_pk_mul_f32 v[52:53], v[74:75], v[52:53]
	s_nop 0
	v_cvt_pk_bf16_f32 v56, v52, v53
	v_lshlrev_b32_e32 v52, 16, v59
	v_and_b32_e32 v53, 0xffff0000, v59
	v_mul_f32_e32 v57, 0xbfb8aa3b, v52
	v_mul_f32_e32 v0, 0xbfb8aa3b, v53
	v_exp_f32_e32 v57, v57
	v_exp_f32_e32 v0, v0
	v_add_f32_e32 v57, 1.0, v57
	v_add_f32_e32 v0, 1.0, v0
	v_rcp_f32_e32 v58, v57
	v_rcp_f32_e32 v59, v0
	s_nop 0
	v_pk_mul_f32 v[52:53], v[58:59], v[52:53]
	s_nop 0
	v_pk_mul_f32 v[52:53], v[52:53], v[70:71]
	s_waitcnt vmcnt(5)
	v_lshlrev_b32_e32 v58, 16, v63
	v_cvt_pk_bf16_f32 v57, v52, v53
	v_add_co_u32_e32 v52, vcc, s3, v68
	v_and_b32_e32 v59, 0xffff0000, v63
	s_nop 0
	v_addc_co_u32_e32 v53, vcc, 0, v69, vcc
	global_store_dwordx4 v[52:53], v[54:57], off
	v_lshlrev_b32_e32 v68, 16, v61
	v_and_b32_e32 v69, 0xffff0000, v61
	s_waitcnt vmcnt(5)
; __device__ __forceinline__ unsigned pk2(float lo, float hi) { const pk_f2 v = {lo, hi}; return __builtin_bit_cast(unsigned, __builtin_convertvector(v, pk_b2)); }
; __device__ __forceinline__ float silu1(float x) { return x * sigmoid_f(x); }
; __device__ __forceinline__ float row16_sum(float v) { v += WS_DPP(v, 0xB1); v += WS_DPP(v, 0x4E); v += WS_DPP(v, 0x141); v += WS_DPP(v, 0x140); return v; }
; __device__ __forceinline__ void phase_hgrn_post(const bf16* O, const bf16* PROJ, const float* ng, bf16* Pb, int gw, int NGW, int lane) {
;     ...
;         for (int j = 0; j < 4; ++j) {
;             const f32x4 o0 = (f32x4){bflo(ob[j].x), bfhi(ob[j].x), bflo(ob[j].y), bfhi(ob[j].y)}, o1 = (f32x4){bflo(ob[j].z), bfhi(ob[j].z), bflo(ob[j].w), bfhi(ob[j].w)};
;             float ss = ((o0.x * o0.x + o0.y * o0.y) + (o0.z * o0.z + o0.w * o0.w)) + ((o1.x * o1.x + o1.y * o1.y) + (o1.z * o1.z + o1.w * o1.w));
;             ss = row16_sum(ss);
;             const float rstd = 1.0f / sqrtf(ss * (1.0f / 128.0f) + EPS);
;             const v4u g = gq[j];
;             v4u w; w.x = pk2(o0.x * rstd * nv[j][0].x * silu1(bflo(g.x)), o0.y * rstd * nv[j][0].y * silu1(bfhi(g.x))); w.y = pk2(o0.z * rstd * nv[j][0].z * silu1(bflo(g.y)), o0.w * rstd * nv[j][0].w * silu1(bfhi(g.y)));
;             w.z = pk2(o1.x * rstd * nv[j][1].x * silu1(bflo(g.z)), o1.y * rstd * nv[j][1].y * silu1(bfhi(g.z))); w.w = pk2(o1.z * rstd * nv[j][1].z * silu1(bflo(g.w)), o1.w * rstd * nv[j][1].w * silu1(bfhi(g.w)));
;             prow[64 * j] = w;
	v_lshlrev_b32_e32 v54, 16, v66
	v_mul_f32_e32 v0, 0xbfb8aa3b, v54
	v_exp_f32_e32 v0, v0
	v_and_b32_e32 v55, 0xffff0000, v66
	v_lshlrev_b32_e32 v56, 16, v62
	v_and_b32_e32 v57, 0xffff0000, v62
	v_add_f32_e32 v0, 1.0, v0
	v_rcp_f32_e32 v62, v0
	v_mul_f32_e32 v0, 0xbfb8aa3b, v55
	v_exp_f32_e32 v0, v0
	v_and_b32_e32 v61, 0xffff0000, v64
	v_mov_b32_e32 v72, v69
	v_mov_b32_e32 v73, v59
	v_add_f32_e32 v0, 1.0, v0
	v_rcp_f32_e32 v63, v0
	v_pk_mul_f32 v[72:73], v[72:73], v[72:73]
	v_mov_b32_e32 v75, v57
	v_pk_mul_f32 v[62:63], v[62:63], v[54:55]
	v_lshlrev_b32_e32 v54, 16, v65
	v_mul_f32_e32 v0, 0xbfb8aa3b, v54
	v_exp_f32_e32 v0, v0
	v_and_b32_e32 v55, 0xffff0000, v65
	v_add_f32_e32 v0, 1.0, v0
	v_rcp_f32_e32 v70, v0
	v_mul_f32_e32 v0, 0xbfb8aa3b, v55
	v_exp_f32_e32 v0, v0
	s_nop 0
	v_add_f32_e32 v0, 1.0, v0
	v_rcp_f32_e32 v71, v0
	s_nop 0
	v_pk_mul_f32 v[70:71], v[70:71], v[54:55]
	v_lshlrev_b32_e32 v54, 16, v60
	v_and_b32_e32 v55, 0xffff0000, v60
	v_lshlrev_b32_e32 v60, 16, v64
	v_mul_f32_e32 v0, 0xbfb8aa3b, v60
	v_exp_f32_e32 v0, v0
	v_mov_b32_e32 v74, v55
	v_pk_mul_f32 v[74:75], v[74:75], v[74:75]
	v_add_f32_e32 v0, 1.0, v0
	v_rcp_f32_e32 v64, v0
	v_mul_f32_e32 v0, 0xbfb8aa3b, v61
	v_exp_f32_e32 v0, v0
	s_nop 0
	v_add_f32_e32 v0, 1.0, v0
	v_rcp_f32_e32 v65, v0
	s_nop 0
	v_pk_mul_f32 v[60:61], v[64:65], v[60:61]
	v_mov_b32_e32 v64, v68
	v_mov_b32_e32 v65, v58
	v_pk_fma_f32 v[64:65], v[64:65], v[64:65], v[72:73]
	v_mov_b32_e32 v72, v54
	v_mov_b32_e32 v73, v56
	v_pk_fma_f32 v[72:73], v[72:73], v[72:73], v[74:75]
	s_nop 0
	v_pk_add_f32 v[64:65], v[72:73], v[64:65]
	s_nop 0
	v_add_f32_e32 v0, v64, v65
	s_nop 1
	v_add_f32_dpp v0, v0, v0 quad_perm:[1,0,3,2] row_mask:0xf bank_mask:0xf bound_ctrl:1
	s_nop 1
	v_add_f32_dpp v0, v0, v0 quad_perm:[2,3,0,1] row_mask:0xf bank_mask:0xf bound_ctrl:1
	s_nop 1
	v_add_f32_dpp v0, v0, v0 row_half_mirror row_mask:0xf bank_mask:0xf bound_ctrl:1
	s_nop 1
	v_add_f32_dpp v0, v0, v0 row_mirror row_mask:0xf bank_mask:0xf bound_ctrl:1
	v_fmamk_f32 v0, v0, 0x3c000000, v192
	v_rsq_f32_e32 v64, v0
	s_nop 0
	v_mul_f32_e32 v65, v0, v64
	v_fma_f32 v65, -v65, v64, 1.0
	v_mul_f32_e32 v66, 0.5, v64
	v_fma_f32 v0, v66, v65, v64
	v_pk_mul_f32 v[54:55], v[0:1], v[54:55] op_sel_hi:[0,1]
	v_pk_mul_f32 v[54:55], v[18:19], v[54:55]
	v_pk_mul_f32 v[56:57], v[0:1], v[56:57] op_sel_hi:[0,1]
	v_pk_mul_f32 v[54:55], v[60:61], v[54:55]
	v_pk_mul_f32 v[60:61], v[0:1], v[68:69] op_sel_hi:[0,1]
	v_pk_mul_f32 v[60:61], v[20:21], v[60:61]
	v_pk_mul_f32 v[56:57], v[22:23], v[56:57]
	v_pk_mul_f32 v[60:61], v[70:71], v[60:61]
	v_cvt_pk_bf16_f32 v54, v54, v55
	v_cvt_pk_bf16_f32 v55, v60, v61
	v_pk_mul_f32 v[56:57], v[62:63], v[56:57]
	v_lshlrev_b32_e32 v60, 16, v67
	v_and_b32_e32 v61, 0xffff0000, v67
	v_cvt_pk_bf16_f32 v56, v56, v57
	v_mul_f32_e32 v57, 0xbfb8aa3b, v60
	v_pk_mul_f32 v[58:59], v[0:1], v[58:59] op_sel_hi:[0,1]
	v_mul_f32_e32 v0, 0xbfb8aa3b, v61
	v_exp_f32_e32 v57, v57
	v_exp_f32_e32 v0, v0
	v_pk_mul_f32 v[58:59], v[24:25], v[58:59]
	v_add_f32_e32 v57, 1.0, v57
	v_add_f32_e32 v0, 1.0, v0
	v_rcp_f32_e32 v62, v57
	v_rcp_f32_e32 v63, v0
	s_nop 0
	v_pk_mul_f32 v[60:61], v[62:63], v[60:61]
	s_nop 0
	v_pk_mul_f32 v[58:59], v[60:61], v[58:59]
	s_waitcnt vmcnt(3)
	v_lshlrev_b32_e32 v60, 16, v43
	v_cvt_pk_bf16_f32 v57, v58, v59
	global_store_dwordx4 v[52:53], v[54:57], off offset:1024
	v_and_b32_e32 v61, 0xffff0000, v43
	s_nop 0
	v_lshlrev_b32_e32 v56, 16, v48
	v_and_b32_e32 v57, 0xffff0000, v48
	v_lshlrev_b32_e32 v48, 16, v44
	v_mul_f32_e32 v0, 0xbfb8aa3b, v48
	v_exp_f32_e32 v0, v0
	v_lshlrev_b32_e32 v54, 16, v49
	v_and_b32_e32 v55, 0xffff0000, v49
	v_and_b32_e32 v49, 0xffff0000, v44
	v_add_f32_e32 v0, 1.0, v0
	v_rcp_f32_e32 v58, v0
	v_mul_f32_e32 v0, 0xbfb8aa3b, v49
	v_exp_f32_e32 v0, v0
	v_mov_b32_e32 v65, v55
	v_mov_b32_e32 v67, v57
	v_add_f32_e32 v0, 1.0, v0
	v_rcp_f32_e32 v59, v0
	v_mul_f32_e32 v0, 0xbfb8aa3b, v60
	v_exp_f32_e32 v0, v0
	v_pk_mul_f32 v[48:49], v[58:59], v[48:49]
	v_lshlrev_b32_e32 v58, 16, v47
	v_add_f32_e32 v0, 1.0, v0
	v_rcp_f32_e32 v62, v0
	v_mul_f32_e32 v0, 0xbfb8aa3b, v61
	v_exp_f32_e32 v0, v0
	v_and_b32_e32 v59, 0xffff0000, v47
	v_and_b32_e32 v47, 0xffff0000, v42
	v_mov_b32_e32 v64, v59
	v_add_f32_e32 v0, 1.0, v0
	v_rcp_f32_e32 v63, v0
	v_pk_mul_f32 v[64:65], v[64:65], v[64:65]
	v_pk_mul_f32 v[60:61], v[62:63], v[60:61]
	v_lshlrev_b32_e32 v62, 16, v46
	v_and_b32_e32 v63, 0xffff0000, v46
	v_lshlrev_b32_e32 v46, 16, v42
	v_mul_f32_e32 v0, 0xbfb8aa3b, v46
	v_exp_f32_e32 v0, v0
	v_mov_b32_e32 v66, v63
	v_pk_mul_f32 v[66:67], v[66:67], v[66:67]
	v_add_f32_e32 v0, 1.0, v0
	v_rcp_f32_e32 v42, v0
	v_mul_f32_e32 v0, 0xbfb8aa3b, v47
	v_exp_f32_e32 v0, v0
	s_nop 0
	v_add_f32_e32 v0, 1.0, v0
	v_rcp_f32_e32 v43, v0
	s_nop 0
	v_pk_mul_f32 v[42:43], v[42:43], v[46:47]
	v_mov_b32_e32 v46, v58
	v_mov_b32_e32 v47, v54
	v_pk_fma_f32 v[46:47], v[46:47], v[46:47], v[64:65]
	v_mov_b32_e32 v64, v62
	v_mov_b32_e32 v65, v56
	v_pk_fma_f32 v[64:65], v[64:65], v[64:65], v[66:67]
	s_nop 0
	v_pk_add_f32 v[46:47], v[64:65], v[46:47]
	s_nop 0
	v_add_f32_e32 v0, v46, v47
	s_nop 1
	v_add_f32_dpp v0, v0, v0 quad_perm:[1,0,3,2] row_mask:0xf bank_mask:0xf bound_ctrl:1
	s_nop 1
	v_add_f32_dpp v0, v0, v0 quad_perm:[2,3,0,1] row_mask:0xf bank_mask:0xf bound_ctrl:1
	s_nop 1
	v_add_f32_dpp v0, v0, v0 row_half_mirror row_mask:0xf bank_mask:0xf bound_ctrl:1
	s_nop 1
	v_add_f32_dpp v0, v0, v0 row_mirror row_mask:0xf bank_mask:0xf bound_ctrl:1
	v_fmamk_f32 v0, v0, 0x3c000000, v192
	v_rsq_f32_e32 v44, v0
	s_nop 0
	v_mul_f32_e32 v46, v0, v44
	v_fma_f32 v46, -v46, v44, 1.0
	v_mul_f32_e32 v47, 0.5, v44
	v_fma_f32 v0, v47, v46, v44
	v_pk_mul_f32 v[46:47], v[0:1], v[62:63] op_sel_hi:[0,1]
	v_pk_mul_f32 v[46:47], v[6:7], v[46:47]
	v_pk_mul_f32 v[54:55], v[0:1], v[54:55] op_sel_hi:[0,1]
	v_pk_mul_f32 v[42:43], v[42:43], v[46:47]
	v_pk_mul_f32 v[46:47], v[0:1], v[58:59] op_sel_hi:[0,1]
	v_pk_mul_f32 v[46:47], v[8:9], v[46:47]
	v_cvt_pk_bf16_f32 v42, v42, v43
	v_pk_mul_f32 v[46:47], v[60:61], v[46:47]
	v_pk_mul_f32 v[54:55], v[16:17], v[54:55]
	v_cvt_pk_bf16_f32 v43, v46, v47
	v_pk_mul_f32 v[46:47], v[0:1], v[56:57] op_sel_hi:[0,1]
	v_pk_mul_f32 v[46:47], v[14:15], v[46:47]
	s_nop 0
	v_pk_mul_f32 v[46:47], v[48:49], v[46:47]
	s_nop 0
	v_cvt_pk_bf16_f32 v44, v46, v47
	v_lshlrev_b32_e32 v46, 16, v45
	v_and_b32_e32 v47, 0xffff0000, v45
	v_mul_f32_e32 v45, 0xbfb8aa3b, v46
	v_mul_f32_e32 v0, 0xbfb8aa3b, v47
	v_exp_f32_e32 v45, v45
	v_exp_f32_e32 v0, v0
	v_add_f32_e32 v45, 1.0, v45
	v_add_f32_e32 v0, 1.0, v0
	v_rcp_f32_e32 v48, v45
	v_rcp_f32_e32 v49, v0
	s_nop 0
	v_pk_mul_f32 v[46:47], v[48:49], v[46:47]
	s_nop 0
	v_pk_mul_f32 v[46:47], v[46:47], v[54:55]
	s_waitcnt vmcnt(2)
; __device__ __forceinline__ unsigned pk2(float lo, float hi) { const pk_f2 v = {lo, hi}; return __builtin_bit_cast(unsigned, __builtin_convertvector(v, pk_b2)); }
; __device__ __forceinline__ float silu1(float x) { return x * sigmoid_f(x); }
; __device__ __forceinline__ float row16_sum(float v) { v += WS_DPP(v, 0xB1); v += WS_DPP(v, 0x4E); v += WS_DPP(v, 0x141); v += WS_DPP(v, 0x140); return v; }
; __device__ __forceinline__ void phase_hgrn_post(const bf16* O, const bf16* PROJ, const float* ng, bf16* Pb, int gw, int NGW, int lane) {
;     ...
;         for (int j = 0; j < 4; ++j) {
;             const f32x4 o0 = (f32x4){bflo(ob[j].x), bfhi(ob[j].x), bflo(ob[j].y), bfhi(ob[j].y)}, o1 = (f32x4){bflo(ob[j].z), bfhi(ob[j].z), bflo(ob[j].w), bfhi(ob[j].w)};
;             float ss = ((o0.x * o0.x + o0.y * o0.y) + (o0.z * o0.z + o0.w * o0.w)) + ((o1.x * o1.x + o1.y * o1.y) + (o1.z * o1.z + o1.w * o1.w));
;             ss = row16_sum(ss);
;             const float rstd = 1.0f / sqrtf(ss * (1.0f / 128.0f) + EPS);
;             const v4u g = gq[j];
;             v4u w; w.x = pk2(o0.x * rstd * nv[j][0].x * silu1(bflo(g.x)), o0.y * rstd * nv[j][0].y * silu1(bfhi(g.x))); w.y = pk2(o0.z * rstd * nv[j][0].z * silu1(bflo(g.y)), o0.w * rstd * nv[j][0].w * silu1(bfhi(g.y)));
;             w.z = pk2(o1.x * rstd * nv[j][1].x * silu1(bflo(g.z)), o1.y * rstd * nv[j][1].y * silu1(bfhi(g.z))); w.w = pk2(o1.z * rstd * nv[j][1].z * silu1(bflo(g.w)), o1.w * rstd * nv[j][1].w * silu1(bfhi(g.w)));
;             prow[64 * j] = w;
;         }
;     }
	v_lshlrev_b32_e32 v48, 16, v35
	v_cvt_pk_bf16_f32 v45, v46, v47
	global_store_dwordx4 v[52:53], v[42:45], off offset:2048
	v_and_b32_e32 v49, 0xffff0000, v35
	s_nop 0
	v_lshlrev_b32_e32 v44, 16, v40
	v_and_b32_e32 v45, 0xffff0000, v40
	v_lshlrev_b32_e32 v40, 16, v36
	v_mul_f32_e32 v0, 0xbfb8aa3b, v40
	v_exp_f32_e32 v0, v0
	v_lshlrev_b32_e32 v42, 16, v41
	v_and_b32_e32 v43, 0xffff0000, v41
	v_and_b32_e32 v41, 0xffff0000, v36
	v_add_f32_e32 v0, 1.0, v0
	v_rcp_f32_e32 v46, v0
	v_mul_f32_e32 v0, 0xbfb8aa3b, v41
	v_exp_f32_e32 v0, v0
	v_mov_b32_e32 v57, v43
	v_mov_b32_e32 v59, v45
	v_add_f32_e32 v0, 1.0, v0
	v_rcp_f32_e32 v47, v0
	v_mul_f32_e32 v0, 0xbfb8aa3b, v48
	v_exp_f32_e32 v0, v0
	v_pk_mul_f32 v[40:41], v[46:47], v[40:41]
	v_lshlrev_b32_e32 v46, 16, v39
	v_add_f32_e32 v0, 1.0, v0
	v_rcp_f32_e32 v54, v0
	v_mul_f32_e32 v0, 0xbfb8aa3b, v49
	v_exp_f32_e32 v0, v0
	v_and_b32_e32 v47, 0xffff0000, v39
	v_and_b32_e32 v39, 0xffff0000, v34
	v_mov_b32_e32 v56, v47
	v_add_f32_e32 v0, 1.0, v0
	v_rcp_f32_e32 v55, v0
	v_pk_mul_f32 v[56:57], v[56:57], v[56:57]
	v_pk_mul_f32 v[48:49], v[54:55], v[48:49]
	v_lshlrev_b32_e32 v54, 16, v38
	v_and_b32_e32 v55, 0xffff0000, v38
	v_lshlrev_b32_e32 v38, 16, v34
	v_mul_f32_e32 v0, 0xbfb8aa3b, v38
	v_exp_f32_e32 v0, v0
	v_mov_b32_e32 v58, v55
	v_pk_mul_f32 v[58:59], v[58:59], v[58:59]
	v_add_f32_e32 v0, 1.0, v0
	v_rcp_f32_e32 v34, v0
	v_mul_f32_e32 v0, 0xbfb8aa3b, v39
	v_exp_f32_e32 v0, v0
	s_nop 0
	v_add_f32_e32 v0, 1.0, v0
	v_rcp_f32_e32 v35, v0
	s_nop 0
	v_pk_mul_f32 v[34:35], v[34:35], v[38:39]
	v_mov_b32_e32 v38, v46
	v_mov_b32_e32 v39, v42
	v_pk_fma_f32 v[38:39], v[38:39], v[38:39], v[56:57]
	v_mov_b32_e32 v56, v54
	v_mov_b32_e32 v57, v44
	v_pk_fma_f32 v[56:57], v[56:57], v[56:57], v[58:59]
	s_nop 0
	v_pk_add_f32 v[38:39], v[56:57], v[38:39]
	s_nop 0
	v_add_f32_e32 v0, v38, v39
	s_nop 1
	v_add_f32_dpp v0, v0, v0 quad_perm:[1,0,3,2] row_mask:0xf bank_mask:0xf bound_ctrl:1
	s_nop 1
	v_add_f32_dpp v0, v0, v0 quad_perm:[2,3,0,1] row_mask:0xf bank_mask:0xf bound_ctrl:1
	s_nop 1
	v_add_f32_dpp v0, v0, v0 row_half_mirror row_mask:0xf bank_mask:0xf bound_ctrl:1
	s_nop 1
	v_add_f32_dpp v0, v0, v0 row_mirror row_mask:0xf bank_mask:0xf bound_ctrl:1
	v_fmamk_f32 v0, v0, 0x3c000000, v192
	v_rsq_f32_e32 v36, v0
	s_nop 0
	v_mul_f32_e32 v38, v0, v36
	v_fma_f32 v38, -v38, v36, 1.0
	v_mul_f32_e32 v39, 0.5, v36
	v_fma_f32 v0, v39, v38, v36
	v_pk_mul_f32 v[38:39], v[0:1], v[54:55] op_sel_hi:[0,1]
	v_pk_mul_f32 v[38:39], v[10:11], v[38:39]
	v_pk_mul_f32 v[42:43], v[0:1], v[42:43] op_sel_hi:[0,1]
	v_pk_mul_f32 v[34:35], v[34:35], v[38:39]
	v_pk_mul_f32 v[38:39], v[0:1], v[46:47] op_sel_hi:[0,1]
	v_pk_mul_f32 v[38:39], v[12:13], v[38:39]
	v_cvt_pk_bf16_f32 v34, v34, v35
	v_pk_mul_f32 v[38:39], v[48:49], v[38:39]
	v_pk_mul_f32 v[42:43], v[4:5], v[42:43]
	v_cvt_pk_bf16_f32 v35, v38, v39
	v_pk_mul_f32 v[38:39], v[0:1], v[44:45] op_sel_hi:[0,1]
	v_pk_mul_f32 v[38:39], v[2:3], v[38:39]
	s_nop 0
	v_pk_mul_f32 v[38:39], v[40:41], v[38:39]
	s_nop 0
	v_cvt_pk_bf16_f32 v36, v38, v39
	v_lshlrev_b32_e32 v38, 16, v37
	v_and_b32_e32 v39, 0xffff0000, v37
	v_mul_f32_e32 v37, 0xbfb8aa3b, v38
	v_mul_f32_e32 v0, 0xbfb8aa3b, v39
	v_exp_f32_e32 v37, v37
	v_exp_f32_e32 v0, v0
	v_add_f32_e32 v37, 1.0, v37
	v_add_f32_e32 v0, 1.0, v0
	v_rcp_f32_e32 v40, v37
	v_rcp_f32_e32 v41, v0
	s_nop 0
	v_pk_mul_f32 v[38:39], v[40:41], v[38:39]
	s_nop 0
	v_pk_mul_f32 v[38:39], v[38:39], v[42:43]
	s_nop 0
	v_cvt_pk_bf16_f32 v37, v38, v39
	global_store_dwordx4 v[52:53], v[34:37], off offset:3072
	s_cbranch_scc0 .LBB0_861

; #define GAS __attribute__((address_space(1)))
; __device__ __forceinline__ float wave_sum(float v) { v = row16_sum(v); return (WS_RL(v, 0) + WS_RL(v, 16)) + (WS_RL(v, 32) + WS_RL(v, 48)); }
; __device__ __forceinline__ void phase_finalnorm_bf(const bf16* hin, const float* g, float* out, int gw, int NGW, int lane) {
;     ...
;         for (int rr = 0; rr < 8; ++rr) {
;             const GAS v4u* xr = (const GAS v4u*)(hin + (size_t)(r0 + rr) * DM) + lane;
;             f32x4 v[8]; float ss = 0.f;
; #pragma unroll
;             for (int j = 0; j < 4; ++j) { const v4u q = xr[64 * j]; v[2 * j] = (f32x4){bflo(q.x), bfhi(q.x), bflo(q.y), bfhi(q.y)}; v[2 * j + 1] = (f32x4){bflo(q.z), bfhi(q.z), bflo(q.w), bfhi(q.w)}; }
; #pragma unroll
;             for (int j = 0; j < 8; ++j) ss += (v[j].x * v[j].x + v[j].y * v[j].y) + (v[j].z * v[j].z + v[j].w * v[j].w);
;             const float rstd = 1.0f / sqrtf(wave_sum(ss) * (1.0f / DM) + EPS);
;             float* orow = out + (size_t)(r0 + rr) * DM + 8 * lane;
; #pragma unroll
;             for (int j = 0; j < 8; ++j) *(GAS f32x4*)(orow + 512 * (j >> 1) + 4 * (j & 1)) = v[j] * rstd * mul[j];
;         }
.LBB0_1086:
	global_load_dwordx4 v[36:39], v[58:59], off offset:-1024
	global_load_dwordx4 v[32:35], v[58:59], off
	global_load_dwordx4 v[40:43], v[58:59], off offset:1024
	global_load_dwordx4 v[44:47], v[58:59], off offset:-2048
	v_lshl_add_u64 v[60:61], v[54:55], 0, s[4:5]
	v_add_co_u32_e32 v80, vcc, s7, v60
	s_add_u32 s4, s4, 0x2000
	s_nop 0
	v_addc_co_u32_e32 v81, vcc, 0, v61, vcc
	s_addc_u32 s5, s5, 0
	v_lshl_add_u64 v[58:59], v[58:59], 0, s[2:3]
	s_cmp_eq_u32 s4, 0x10000
	s_waitcnt vmcnt(3)
	v_lshlrev_b32_e32 v64, 16, v38
	v_and_b32_e32 v65, 0xffff0000, v38
	s_waitcnt vmcnt(2)
	v_lshlrev_b32_e32 v38, 16, v32
	s_waitcnt vmcnt(0)
	v_lshlrev_b32_e32 v69, 16, v46
	v_and_b32_e32 v71, 0xffff0000, v46
	v_and_b32_e32 v70, 0xffff0000, v44
	v_lshlrev_b32_e32 v73, 16, v47
	v_and_b32_e32 v47, 0xffff0000, v47
	v_and_b32_e32 v46, 0xffff0000, v45
	v_lshlrev_b32_e32 v68, 16, v44
	v_lshlrev_b32_e32 v72, 16, v45
	v_lshlrev_b32_e32 v45, 16, v37
	v_lshlrev_b32_e32 v44, 16, v36
	v_and_b32_e32 v37, 0xffff0000, v37
	v_and_b32_e32 v36, 0xffff0000, v36
	v_pk_mul_f32 v[82:83], v[70:71], v[70:71]
	v_pk_mul_f32 v[84:85], v[46:47], v[46:47]
	v_lshlrev_b32_e32 v74, 16, v39
	v_pk_mul_f32 v[86:87], v[36:37], v[36:37]
	v_mov_b32_e32 v102, v68
	v_mov_b32_e32 v103, v70
	v_mov_b32_e32 v104, v72
	v_mov_b32_e32 v105, v46
	v_mov_b32_e32 v70, v69
	v_mov_b32_e32 v46, v73
	v_pk_fma_f32 v[68:69], v[68:69], v[68:69], v[82:83]
	v_pk_fma_f32 v[72:73], v[72:73], v[72:73], v[84:85]
	v_and_b32_e32 v91, 0xffff0000, v32
	v_and_b32_e32 v75, 0xffff0000, v39
	v_lshlrev_b32_e32 v77, 16, v35
	v_lshlrev_b32_e32 v76, 16, v34
	v_and_b32_e32 v35, 0xffff0000, v35
	v_and_b32_e32 v34, 0xffff0000, v34
	v_mul_f32_e32 v39, v64, v64
	v_mul_f32_e32 v89, v65, v65
	v_mul_f32_e32 v90, v74, v74
	v_mov_b32_e32 v88, v38
	v_mov_b32_e32 v106, v44
	v_mov_b32_e32 v107, v36
	v_mov_b32_e32 v36, v45
	v_pk_fma_f32 v[44:45], v[44:45], v[44:45], v[86:87]
	v_pk_add_f32 v[68:69], v[68:69], v[72:73]
	v_lshlrev_b32_e32 v32, 16, v33
	v_and_b32_e32 v33, 0xffff0000, v33
	v_pk_mul_f32 v[94:95], v[34:35], v[34:35]
	v_pk_fma_f32 v[82:83], v[74:75], v[74:75], v[90:91] op_sel_hi:[1,1,0]
	v_pk_add_f32 v[84:85], v[38:39], v[88:89]
	v_pk_add_f32 v[44:45], v[44:45], v[44:45] op_sel_hi:[0,1]
	v_pk_add_f32 v[68:69], v[68:69], v[68:69] op_sel_hi:[0,1]
	v_mul_f32_e32 v92, v38, v38
	v_mov_b32_e32 v108, v76
	v_mov_b32_e32 v109, v34
	v_mov_b32_e32 v34, v77
	v_pk_fma_f32 v[76:77], v[76:77], v[76:77], v[94:95]
	v_mul_f32_e32 v82, v91, v91
	v_mov_b32_e32 v93, v85
	v_mul_f32_e32 v44, v33, v33
	v_mul_f32_e32 v68, v32, v32
	v_lshlrev_b32_e32 v66, 16, v40
	v_and_b32_e32 v67, 0xffff0000, v40
	v_lshlrev_b32_e32 v40, 16, v42
	v_lshlrev_b32_e32 v78, 16, v41
	v_pk_add_f32 v[72:73], v[76:77], v[76:77] op_sel_hi:[0,1]
	v_pk_add_f32 v[76:77], v[92:93], v[82:83]
	v_pk_add_f32 v[44:45], v[68:69], v[44:45]
	v_and_b32_e32 v99, 0xffff0000, v42
	v_and_b32_e32 v79, 0xffff0000, v41
	v_mul_f32_e32 v41, v66, v66
	v_mul_f32_e32 v97, v67, v67
	v_mul_f32_e32 v98, v78, v78
	v_mov_b32_e32 v96, v40
	v_pk_add_f32 v[44:45], v[76:77], v[44:45]
	v_lshlrev_b32_e32 v42, 16, v43
	v_and_b32_e32 v43, 0xffff0000, v43
	v_pk_fma_f32 v[86:87], v[78:79], v[78:79], v[98:99] op_sel_hi:[1,1,0]
	v_pk_add_f32 v[88:89], v[40:41], v[96:97]
	v_pk_add_f32 v[44:45], v[44:45], v[44:45] op_sel_hi:[0,1]
	v_mul_f32_e32 v100, v40, v40
	v_mul_f32_e32 v86, v99, v99
	v_mov_b32_e32 v101, v89
	v_mul_f32_e32 v72, v42, v42
	v_mul_f32_e32 v44, v43, v43
	v_pk_add_f32 v[82:83], v[100:101], v[86:87]
	v_pk_add_f32 v[44:45], v[72:73], v[44:45]
	v_mov_b32_e32 v39, v91
	v_pk_add_f32 v[44:45], v[82:83], v[44:45]
	v_mov_b32_e32 v41, v99
	v_add_f32_e32 v44, v44, v45
	s_nop 1
	v_add_f32_dpp v44, v44, v44 quad_perm:[1,0,3,2] row_mask:0xf bank_mask:0xf bound_ctrl:1
	s_nop 1
	v_add_f32_dpp v44, v44, v44 quad_perm:[2,3,0,1] row_mask:0xf bank_mask:0xf bound_ctrl:1
	s_nop 1
	v_add_f32_dpp v44, v44, v44 row_half_mirror row_mask:0xf bank_mask:0xf bound_ctrl:1
	s_nop 1
	v_add_f32_dpp v44, v44, v44 row_mirror row_mask:0xf bank_mask:0xf bound_ctrl:1
	s_nop 0
	v_readlane_b32 s8, v44, 16
	v_readlane_b32 s9, v44, 48
	v_readlane_b32 s0, v44, 0
	v_readlane_b32 s1, v44, 32
	v_mov_b32_e32 v44, s8
	v_mov_b32_e32 v45, s9
	v_pk_add_f32 v[44:45], s[0:1], v[44:45]
	s_nop 0
	v_add_f32_e32 v44, v44, v45
	v_fmamk_f32 v44, v44, 0x3a000000, v62
	v_mul_f32_e32 v45, 0x4f800000, v44
	v_rsq_f32_e32 v45, v44
	s_nop 0
	v_mul_f32_e32 v68, v44, v45
	v_fma_f32 v68, -v68, v45, 1.0
	v_mul_f32_e32 v69, 0.5, v45
	v_fma_f32 v44, v69, v68, v45
	v_pk_mul_f32 v[68:69], v[102:103], v[44:45] op_sel_hi:[1,0]
	v_pk_mul_f32 v[72:73], v[104:105], v[44:45] op_sel_hi:[1,0]
	v_pk_mul_f32 v[70:71], v[70:71], v[44:45] op_sel_hi:[1,0]
	v_pk_mul_f32 v[46:47], v[46:47], v[44:45] op_sel_hi:[1,0]
	v_pk_mul_f32 v[76:77], v[44:45], v[106:107] op_sel_hi:[0,1]
	v_pk_mul_f32 v[82:83], v[44:45], v[36:37] op_sel_hi:[0,1]
	v_pk_mul_f32 v[64:65], v[64:65], v[44:45] op_sel_hi:[1,0]
	v_pk_mul_f32 v[74:75], v[74:75], v[44:45] op_sel_hi:[1,0]
	v_pk_mul_f32 v[84:85], v[38:39], v[44:45] op_sel_hi:[1,0]
	v_pk_mul_f32 v[86:87], v[32:33], v[44:45] op_sel_hi:[1,0]
	v_pk_mul_f32 v[88:89], v[44:45], v[108:109] op_sel_hi:[0,1]
	v_pk_mul_f32 v[90:91], v[44:45], v[34:35] op_sel_hi:[0,1]
	v_pk_mul_f32 v[92:93], v[66:67], v[44:45] op_sel_hi:[1,0]
	v_pk_mul_f32 v[78:79], v[78:79], v[44:45] op_sel_hi:[1,0]
	v_pk_mul_f32 v[94:95], v[40:41], v[44:45] op_sel_hi:[1,0]
	v_pk_mul_f32 v[96:97], v[42:43], v[44:45] op_sel_hi:[1,0]
	v_pk_mul_f32 v[34:35], v[6:7], v[72:73]
	v_pk_mul_f32 v[32:33], v[4:5], v[68:69]
	v_pk_mul_f32 v[38:39], v[2:3], v[46:47]
	v_pk_mul_f32 v[36:37], v[0:1], v[70:71]
	v_pk_mul_f32 v[42:43], v[14:15], v[82:83]
	v_pk_mul_f32 v[40:41], v[12:13], v[76:77]
	v_pk_mul_f32 v[46:47], v[10:11], v[74:75]
	v_pk_mul_f32 v[44:45], v[8:9], v[64:65]
	v_pk_mul_f32 v[66:67], v[22:23], v[86:87]
	v_pk_mul_f32 v[64:65], v[20:21], v[84:85]
	v_pk_mul_f32 v[70:71], v[18:19], v[90:91]
	v_pk_mul_f32 v[68:69], v[16:17], v[88:89]
	v_pk_mul_f32 v[74:75], v[30:31], v[78:79]
	v_pk_mul_f32 v[72:73], v[28:29], v[92:93]
	v_pk_mul_f32 v[78:79], v[26:27], v[96:97]
	v_pk_mul_f32 v[76:77], v[24:25], v[94:95]
	global_store_dwordx4 v[60:61], v[32:35], off
	global_store_dwordx4 v[60:61], v[36:39], off offset:16
	global_store_dwordx4 v[60:61], v[40:43], off offset:2048
	global_store_dwordx4 v[60:61], v[44:47], off offset:2064
	global_store_dwordx4 v[80:81], v[64:67], off
	global_store_dwordx4 v[80:81], v[68:71], off offset:16
	global_store_dwordx4 v[80:81], v[72:75], off offset:2048
	global_store_dwordx4 v[80:81], v[76:79], off offset:2064
	s_cbranch_scc0 .LBB0_1086
	s_add_i32 s10, s10, s88
	v_lshl_add_u64 v[54:55], v[54:55], 0, s[24:25]
	s_cmpk_gt_i32 s10, 0x3fff
	v_lshl_add_u64 v[56:57], v[56:57], 0, s[20:21]
	s_cbranch_scc0 .LBB0_1085
